# P4 MoE loops: removed wave-uniform nmf exec-mask diamonds (MFMA groups unconditional); attention mask block pipelined; P4 setup loads overlapped
# speedup vs baseline: 1.0199x; 1.0080x over previous
.LBB0_715:
	s_add_i32 s38, s71, -1
	s_bitcmp1_b32 s38, 0
	s_cselect_b32 s39, 0x3400, 0
	v_add_u32_e32 v66, s39, v166
	ds_read_b128 v[10:13], v66
	ds_read_b128 v[14:17], v66 offset:32
	ds_read_b128 v[142:145], v66 offset:6656
	ds_read_b128 v[146:149], v66 offset:6688
	ds_read_b128 v[150:153], v66 offset:64
	ds_read_b128 v[154:157], v66 offset:96
	ds_read_b128 v[168:171], v66 offset:6720
	ds_read_b128 v[172:175], v66 offset:6752
	ds_read_b128 v[176:179], v66 offset:128
	ds_read_b128 v[180:183], v66 offset:160
	ds_read_b128 v[184:187], v66 offset:6784
	ds_read_b128 v[188:191], v66 offset:6816
	s_waitcnt lgkmcnt(11)
	v_mfma_f32_32x32x16_bf16 v[82:97], v[10:13], v[98:101], v[50:65]
	s_cmp_lt_u32 s38, s72
	s_waitcnt lgkmcnt(9)
	v_mfma_f32_32x32x16_bf16 v[66:81], v[142:145], v[98:101], v[50:65]
	v_mfma_f32_32x32x16_bf16 v[82:97], v[14:17], v[102:105], v[82:97]
	s_waitcnt lgkmcnt(8)
	v_mfma_f32_32x32x16_bf16 v[66:81], v[146:149], v[102:105], v[66:81]
	s_waitcnt lgkmcnt(7)
	v_mfma_f32_32x32x16_bf16 v[82:97], v[150:153], v[106:109], v[82:97]
	s_waitcnt lgkmcnt(5)
	v_mfma_f32_32x32x16_bf16 v[66:81], v[168:171], v[106:109], v[66:81]
	v_mfma_f32_32x32x16_bf16 v[82:97], v[154:157], v[110:113], v[82:97]
	s_waitcnt lgkmcnt(4)
	v_mfma_f32_32x32x16_bf16 v[66:81], v[172:175], v[110:113], v[66:81]
	s_waitcnt lgkmcnt(3)
	v_mfma_f32_32x32x16_bf16 v[82:97], v[176:179], v[114:117], v[82:97]
	s_waitcnt lgkmcnt(1)
	v_mfma_f32_32x32x16_bf16 v[66:81], v[184:187], v[114:117], v[66:81]
	v_mfma_f32_32x32x16_bf16 v[82:97], v[180:183], v[118:121], v[82:97]
	s_waitcnt lgkmcnt(0)
	v_mfma_f32_32x32x16_bf16 v[66:81], v[188:191], v[118:121], v[66:81]
	s_nop 15
	s_nop 7
	s_cbranch_scc1 .LBB0_717
	v_add3_u32 v10, s12, v167, 64
	v_sub_u32_e32 v10, v134, v10
	v_cmp_le_i32_e32 vcc, 0, v10
	v_cmp_le_i32_e64 s[38:39], 32, v10
	v_cmp_le_i32_e64 s[78:79], 1, v10
	v_cndmask_b32_e32 v82, v221, v82, vcc
	v_cmp_le_i32_e32 vcc, 33, v10
	v_cndmask_b32_e64 v66, v221, v66, s[38:39]
	v_cmp_le_i32_e64 s[38:39], 2, v10
	v_cndmask_b32_e64 v83, v221, v83, s[78:79]
	v_cmp_le_i32_e64 s[78:79], 34, v10
	v_cndmask_b32_e32 v67, v221, v67, vcc
	v_cmp_le_i32_e32 vcc, 3, v10
	v_cndmask_b32_e64 v84, v221, v84, s[38:39]
	v_cmp_le_i32_e64 s[38:39], 35, v10
	v_cndmask_b32_e64 v68, v221, v68, s[78:79]
	v_cmp_le_i32_e64 s[78:79], 8, v10
	v_cndmask_b32_e32 v85, v221, v85, vcc
	v_cmp_le_i32_e32 vcc, 40, v10
	v_cndmask_b32_e64 v69, v221, v69, s[38:39]
	v_cmp_le_i32_e64 s[38:39], 9, v10
	v_cndmask_b32_e64 v86, v221, v86, s[78:79]
	v_cmp_le_i32_e64 s[78:79], 41, v10
	v_cndmask_b32_e32 v70, v221, v70, vcc
	v_cmp_le_i32_e32 vcc, 10, v10
	v_cndmask_b32_e64 v87, v221, v87, s[38:39]
	v_cmp_le_i32_e64 s[38:39], 42, v10
	v_cndmask_b32_e64 v71, v221, v71, s[78:79]
	v_cmp_le_i32_e64 s[78:79], 11, v10
	v_cndmask_b32_e32 v88, v221, v88, vcc
	v_cmp_le_i32_e32 vcc, 43, v10
	v_cndmask_b32_e64 v72, v221, v72, s[38:39]
	v_cmp_le_i32_e64 s[38:39], 16, v10
	v_cndmask_b32_e64 v89, v221, v89, s[78:79]
	v_cmp_le_i32_e64 s[78:79], 48, v10
	v_cndmask_b32_e32 v73, v221, v73, vcc
	v_cmp_le_i32_e32 vcc, 17, v10
	v_cndmask_b32_e64 v90, v221, v90, s[38:39]
	v_cmp_le_i32_e64 s[38:39], 49, v10
	v_cndmask_b32_e64 v74, v221, v74, s[78:79]
	v_cmp_le_i32_e64 s[78:79], 18, v10
	v_cndmask_b32_e32 v91, v221, v91, vcc
	v_cmp_le_i32_e32 vcc, 50, v10
	v_cndmask_b32_e64 v75, v221, v75, s[38:39]
	v_cmp_le_i32_e64 s[38:39], 19, v10
	v_cndmask_b32_e64 v92, v221, v92, s[78:79]
	v_cmp_le_i32_e64 s[78:79], 51, v10
	v_cndmask_b32_e32 v76, v221, v76, vcc
	v_cmp_le_i32_e32 vcc, 24, v10
	v_cndmask_b32_e64 v93, v221, v93, s[38:39]
	v_cmp_le_i32_e64 s[38:39], 56, v10
	v_cndmask_b32_e64 v77, v221, v77, s[78:79]
	v_cmp_le_i32_e64 s[78:79], 25, v10
	v_cndmask_b32_e32 v94, v221, v94, vcc
	v_cmp_le_i32_e32 vcc, 57, v10
	v_cndmask_b32_e64 v78, v221, v78, s[38:39]
	v_cmp_le_i32_e64 s[38:39], 26, v10
	v_cndmask_b32_e64 v95, v221, v95, s[78:79]
	v_cmp_le_i32_e64 s[78:79], 58, v10
	v_cndmask_b32_e32 v79, v221, v79, vcc
	v_cmp_le_i32_e32 vcc, 27, v10
	v_cndmask_b32_e64 v96, v221, v96, s[38:39]
	v_cmp_le_i32_e64 s[38:39], 59, v10
	v_cndmask_b32_e64 v80, v221, v80, s[78:79]
	v_cndmask_b32_e32 v97, v221, v97, vcc
	v_cndmask_b32_e64 v81, v221, v81, s[38:39]

.LBB0_763:
	s_add_i32 s38, s55, -1
	s_bitcmp1_b32 s38, 0
	s_cselect_b32 s39, 0x3400, 0
	v_add_u32_e32 v66, s39, v166
	ds_read_b128 v[10:13], v66
	ds_read_b128 v[14:17], v66 offset:32
	ds_read_b128 v[142:145], v66 offset:6656
	ds_read_b128 v[146:149], v66 offset:6688
	ds_read_b128 v[150:153], v66 offset:64
	ds_read_b128 v[154:157], v66 offset:96
	ds_read_b128 v[168:171], v66 offset:6720
	ds_read_b128 v[172:175], v66 offset:6752
	ds_read_b128 v[176:179], v66 offset:128
	ds_read_b128 v[180:183], v66 offset:160
	ds_read_b128 v[184:187], v66 offset:6784
	ds_read_b128 v[188:191], v66 offset:6816
	s_waitcnt lgkmcnt(11)
	v_mfma_f32_32x32x16_bf16 v[82:97], v[10:13], v[98:101], v[50:65]
	s_cmp_lt_u32 s38, s58
	s_waitcnt lgkmcnt(9)
	v_mfma_f32_32x32x16_bf16 v[66:81], v[142:145], v[98:101], v[50:65]
	v_mfma_f32_32x32x16_bf16 v[82:97], v[14:17], v[102:105], v[82:97]
	s_waitcnt lgkmcnt(8)
	v_mfma_f32_32x32x16_bf16 v[66:81], v[146:149], v[102:105], v[66:81]
	s_waitcnt lgkmcnt(7)
	v_mfma_f32_32x32x16_bf16 v[82:97], v[150:153], v[106:109], v[82:97]
	s_waitcnt lgkmcnt(5)
	v_mfma_f32_32x32x16_bf16 v[66:81], v[168:171], v[106:109], v[66:81]
	v_mfma_f32_32x32x16_bf16 v[82:97], v[154:157], v[110:113], v[82:97]
	s_waitcnt lgkmcnt(4)
	v_mfma_f32_32x32x16_bf16 v[66:81], v[172:175], v[110:113], v[66:81]
	s_waitcnt lgkmcnt(3)
	v_mfma_f32_32x32x16_bf16 v[82:97], v[176:179], v[114:117], v[82:97]
	s_waitcnt lgkmcnt(1)
	v_mfma_f32_32x32x16_bf16 v[66:81], v[184:187], v[114:117], v[66:81]
	v_mfma_f32_32x32x16_bf16 v[82:97], v[180:183], v[118:121], v[82:97]
	s_waitcnt lgkmcnt(0)
	v_mfma_f32_32x32x16_bf16 v[66:81], v[188:191], v[118:121], v[66:81]
	s_nop 15
	s_nop 7
	s_cbranch_scc1 .LBB0_765
	v_add3_u32 v10, s12, v167, 64
	v_sub_u32_e32 v10, v134, v10
	v_cmp_le_i32_e32 vcc, 0, v10
	v_cmp_le_i32_e64 s[38:39], 32, v10
	v_cmp_le_i32_e64 s[78:79], 1, v10
	v_cndmask_b32_e32 v82, v221, v82, vcc
	v_cmp_le_i32_e32 vcc, 33, v10
	v_cndmask_b32_e64 v66, v221, v66, s[38:39]
	v_cmp_le_i32_e64 s[38:39], 2, v10
	v_cndmask_b32_e64 v83, v221, v83, s[78:79]
	v_cmp_le_i32_e64 s[78:79], 34, v10
	v_cndmask_b32_e32 v67, v221, v67, vcc
	v_cmp_le_i32_e32 vcc, 3, v10
	v_cndmask_b32_e64 v84, v221, v84, s[38:39]
	v_cmp_le_i32_e64 s[38:39], 35, v10
	v_cndmask_b32_e64 v68, v221, v68, s[78:79]
	v_cmp_le_i32_e64 s[78:79], 8, v10
	v_cndmask_b32_e32 v85, v221, v85, vcc
	v_cmp_le_i32_e32 vcc, 40, v10
	v_cndmask_b32_e64 v69, v221, v69, s[38:39]
	v_cmp_le_i32_e64 s[38:39], 9, v10
	v_cndmask_b32_e64 v86, v221, v86, s[78:79]
	v_cmp_le_i32_e64 s[78:79], 41, v10
	v_cndmask_b32_e32 v70, v221, v70, vcc
	v_cmp_le_i32_e32 vcc, 10, v10
	v_cndmask_b32_e64 v87, v221, v87, s[38:39]
	v_cmp_le_i32_e64 s[38:39], 42, v10
	v_cndmask_b32_e64 v71, v221, v71, s[78:79]
	v_cmp_le_i32_e64 s[78:79], 11, v10
	v_cndmask_b32_e32 v88, v221, v88, vcc
	v_cmp_le_i32_e32 vcc, 43, v10
	v_cndmask_b32_e64 v72, v221, v72, s[38:39]
	v_cmp_le_i32_e64 s[38:39], 16, v10
	v_cndmask_b32_e64 v89, v221, v89, s[78:79]
	v_cmp_le_i32_e64 s[78:79], 48, v10
	v_cndmask_b32_e32 v73, v221, v73, vcc
	v_cmp_le_i32_e32 vcc, 17, v10
	v_cndmask_b32_e64 v90, v221, v90, s[38:39]
	v_cmp_le_i32_e64 s[38:39], 49, v10
	v_cndmask_b32_e64 v74, v221, v74, s[78:79]
	v_cmp_le_i32_e64 s[78:79], 18, v10
	v_cndmask_b32_e32 v91, v221, v91, vcc
	v_cmp_le_i32_e32 vcc, 50, v10
	v_cndmask_b32_e64 v75, v221, v75, s[38:39]
	v_cmp_le_i32_e64 s[38:39], 19, v10
	v_cndmask_b32_e64 v92, v221, v92, s[78:79]
	v_cmp_le_i32_e64 s[78:79], 51, v10
	v_cndmask_b32_e32 v76, v221, v76, vcc
	v_cmp_le_i32_e32 vcc, 24, v10
	v_cndmask_b32_e64 v93, v221, v93, s[38:39]
	v_cmp_le_i32_e64 s[38:39], 56, v10
	v_cndmask_b32_e64 v77, v221, v77, s[78:79]
	v_cmp_le_i32_e64 s[78:79], 25, v10
	v_cndmask_b32_e32 v94, v221, v94, vcc
	v_cmp_le_i32_e32 vcc, 57, v10
	v_cndmask_b32_e64 v78, v221, v78, s[38:39]
	v_cmp_le_i32_e64 s[38:39], 26, v10
	v_cndmask_b32_e64 v95, v221, v95, s[78:79]
	v_cmp_le_i32_e64 s[78:79], 58, v10
	v_cndmask_b32_e32 v79, v221, v79, vcc
	v_cmp_le_i32_e32 vcc, 27, v10
	v_cndmask_b32_e64 v96, v221, v96, s[38:39]
	v_cmp_le_i32_e64 s[38:39], 59, v10
	v_cndmask_b32_e64 v80, v221, v80, s[78:79]
	v_cndmask_b32_e32 v97, v221, v97, vcc
	v_cndmask_b32_e64 v81, v221, v81, s[38:39]

.LBB0_1253:
	s_or_b32 s12, s12, s72
	v_cmp_lt_i32_e32 vcc, s12, v228
	s_or_b64 s[58:59], s[58:59], exec
	s_and_saveexec_b64 s[60:61], vcc
	s_cbranch_execz .LBB0_1252
	v_cmp_ge_i32_e64 s[38:39], s12, v227
	s_bcnt1_i32_b32 s64, s38
	v_and_or_b32 v3, s64, 31, v226
	v_lshlrev_b32_e32 v3, 2, v3
	ds_bpermute_b32 v3, v3, v225
	s_mov_b32 s18, 0x38e38e39
	v_sub_u32_e64 v4, s64, 1 clamp
	v_add_lshl_u32 v4, v4, v226, 2
	ds_bpermute_b32 v4, v4, v227
	s_waitcnt lgkmcnt(1)
	v_add_u32_e32 v5, 0x8f, v3
	v_mul_hi_i32 v5, v5, s18
	v_lshrrev_b32_e32 v6, 31, v5
	v_ashrrev_i32_e32 v5, 5, v5
	v_add_u32_e32 v5, v5, v6
	v_sub_u32_e32 v6, 0, v5
	v_max_i32_e32 v6, v5, v6
	v_cvt_f32_u32_e32 v7, v6
	v_add3_u32 v8, v3, v5, -1
	v_sub_u32_e32 v9, 0, v8
	v_xor_b32_e32 v5, v8, v5
	v_rcp_iflag_f32_e32 v7, v7
	v_max_i32_e32 v8, v8, v9
	v_sub_u32_e32 v9, 0, v6
	s_mov_b32 s39, s21
	v_mul_f32_e32 v7, 0x4f7ffffe, v7
	v_cvt_u32_f32_e32 v7, v7
	s_cmp_lg_u64 s[38:39], 0
	s_cselect_b64 vcc, -1, 0
	s_waitcnt lgkmcnt(0)
	v_cndmask_b32_e32 v4, 0, v4, vcc
	v_mul_lo_u32 v9, v9, v7
	v_mul_hi_u32 v9, v7, v9
	v_add_u32_e32 v7, v7, v9
	v_mul_hi_u32 v7, v8, v7
	v_mul_lo_u32 v9, v7, v6
	v_sub_u32_e32 v8, v8, v9
	v_add_u32_e32 v9, 1, v7
	v_cmp_ge_u32_e32 vcc, v8, v6
	v_ashrrev_i32_e32 v5, 31, v5
	v_sub_u32_e32 v4, s12, v4
	v_cndmask_b32_e32 v7, v7, v9, vcc
	v_sub_u32_e32 v9, v8, v6
	v_cndmask_b32_e32 v8, v8, v9, vcc
	v_add_u32_e32 v9, 1, v7
	v_cmp_ge_u32_e32 vcc, v8, v6
	s_barrier
	s_nop 0
	v_cndmask_b32_e32 v6, v7, v9, vcc
	v_xor_b32_e32 v6, v6, v5
	v_sub_u32_e32 v5, v6, v5
	v_mul_lo_u32 v4, v4, v5
	v_sub_u32_e32 v3, v3, v4
	v_min_i32_e32 v3, v5, v3
	s_and_saveexec_b64 s[38:39], s[40:41]
	s_cbranch_execz .LBB0_1256
	s_lshl_b32 s12, s64, 17
	v_readlane_b32 s18, v251, 61
	v_cmp_lt_i32_e32 vcc, v224, v3
	v_readlane_b32 s19, v251, 62
	s_add_u32 s42, s18, s12
	v_ashrrev_i32_e32 v5, 31, v4
	v_cndmask_b32_e32 v6, 0, v224, vcc
	s_addc_u32 s43, s19, 0
	v_ashrrev_i32_e32 v7, 31, v6
	v_lshl_add_u64 v[4:5], v[4:5], 2, s[42:43]
	v_lshl_add_u64 v[4:5], v[6:7], 2, v[4:5]
	global_load_dword v4, v[4:5], off
	v_readlane_b32 s18, v251, 63
	v_readlane_b32 s19, v247, 0
	s_waitcnt vmcnt(0)
	v_ashrrev_i32_e32 v5, 31, v4
	v_ashrrev_i32_e32 v6, 1, v4
	v_cndmask_b32_e32 v7, -1, v4, vcc
	v_lshl_add_u64 v[4:5], v[4:5], 2, s[18:19]
	global_load_dword v4, v[4:5], off
	v_readlane_b32 s18, v247, 1
	ds_write_b32 v230, v7
	v_ashrrev_i32_e32 v7, 31, v6
	v_readlane_b32 s19, v247, 2
	ds_write_b32 v229, v6
	s_nop 1
	v_lshl_add_u64 v[8:9], v[6:7], 2, s[18:19]
	global_load_dword v8, v[8:9], off
	s_waitcnt vmcnt(1)
	ds_write_b32 v231, v4
	s_waitcnt vmcnt(0)
	ds_write_b32 v232, v8

.LBB0_1264:
	ds_read_b128 v[198:201], v238
	ds_read_b128 v[194:197], v238 offset:4096
	ds_read_b128 v[202:205], v238 offset:8192
	ds_read_b128 v[18:21], v238 offset:12288
	ds_read_b128 v[22:25], v238 offset:16384
	ds_read_b128 v[34:37], v238 offset:20480
.LBB0_1266:
	v_lshl_or_b32 v4, s67, 7, v234
	v_ashrrev_i32_e32 v5, 31, v4
	ds_read2_b32 v[124:125], v233 offset1:32
	v_lshlrev_b64 v[122:123], 1, v[4:5]
	s_waitcnt lgkmcnt(0)
	v_ashrrev_i32_e32 v127, 31, v124
	v_mov_b32_e32 v126, v124
	v_ashrrev_i32_e32 v129, 31, v125
	v_mov_b32_e32 v128, v125
	v_lshlrev_b64 v[124:125], 11, v[126:127]
	v_lshlrev_b64 v[126:127], 11, v[128:129]
	v_lshl_add_u64 v[124:125], s[6:7], 0, v[124:125]
	v_lshl_add_u64 v[126:127], s[6:7], 0, v[126:127]
	v_lshl_add_u64 v[124:125], v[124:125], 0, v[122:123]
	v_lshl_add_u64 v[126:127], v[126:127], 0, v[122:123]
	global_load_dwordx4 v[142:145], v[124:125], off
	s_nop 0
	global_load_dwordx4 v[126:129], v[126:127], off
	s_waitcnt vmcnt(9)
	v_mfma_f32_16x16x32_bf16 v[182:185], v[166:169], v[198:201], v[182:185]
	s_waitcnt vmcnt(5)
	v_mfma_f32_16x16x32_bf16 v[162:165], v[174:177], v[198:201], v[162:165]
	v_mfma_f32_16x16x32_bf16 v[134:137], v[166:169], v[194:197], v[134:137]
	v_mfma_f32_16x16x32_bf16 v[118:121], v[174:177], v[194:197], v[118:121]
	v_mfma_f32_16x16x32_bf16 v[102:105], v[166:169], v[202:205], v[102:105]
	v_mfma_f32_16x16x32_bf16 v[86:89], v[174:177], v[202:205], v[86:89]
.LBB0_1268:
	ds_read_b128 v[194:197], v238 offset:28672
	ds_read_b128 v[198:201], v238 offset:24576
	ds_read_b128 v[202:205], v238 offset:32768
.LBB0_1270:
	ds_read2_b32 v[124:125], v233 offset0:64 offset1:96
	s_waitcnt lgkmcnt(0)
	v_ashrrev_i32_e32 v131, 31, v124
	v_mov_b32_e32 v130, v124
	v_ashrrev_i32_e32 v133, 31, v125
	v_mov_b32_e32 v132, v125
	v_lshlrev_b64 v[124:125], 11, v[130:131]
	v_lshlrev_b64 v[130:131], 11, v[132:133]
	v_lshl_add_u64 v[124:125], s[6:7], 0, v[124:125]
	v_lshl_add_u64 v[130:131], s[6:7], 0, v[130:131]
	v_lshl_add_u64 v[124:125], v[124:125], 0, v[122:123]
	v_lshl_add_u64 v[122:123], v[130:131], 0, v[122:123]
	global_load_dwordx4 v[130:133], v[124:125], off
	s_nop 0
	global_load_dwordx4 v[122:125], v[122:123], off
	s_waitcnt vmcnt(11)
	v_mfma_f32_16x16x32_bf16 v[82:85], v[166:169], v[18:21], v[82:85]
	s_waitcnt vmcnt(7)
	v_mfma_f32_16x16x32_bf16 v[78:81], v[174:177], v[18:21], v[78:81]
	v_mfma_f32_16x16x32_bf16 v[74:77], v[166:169], v[22:25], v[74:77]
	v_mfma_f32_16x16x32_bf16 v[70:73], v[174:177], v[22:25], v[70:73]
	v_mfma_f32_16x16x32_bf16 v[66:69], v[166:169], v[34:37], v[66:69]
	v_mfma_f32_16x16x32_bf16 v[62:65], v[174:177], v[34:37], v[62:65]
.LBB0_1272:
	ds_read_b128 v[18:21], v241
	ds_read_b128 v[22:25], v241 offset:4096
	ds_read_b128 v[34:37], v241 offset:8192
.LBB0_1274:
	s_and_saveexec_b64 s[38:39], s[48:49]
	s_cbranch_execz .LBB0_1276
	ds_read_b32 v6, v233 offset:512
	s_waitcnt lgkmcnt(0)
	v_ashrrev_i32_e32 v7, 31, v6
	v_lshlrev_b64 v[6:7], 11, v[6:7]
	v_lshl_add_u64 v[6:7], s[6:7], 0, v[6:7]
	v_lshl_add_u64 v[4:5], v[4:5], 1, v[6:7]
	global_load_dwordx4 v[6:9], v[4:5], off
.LBB0_1276:
	s_or_b64 exec, exec, s[38:39]
	s_waitcnt vmcnt(11)
	v_mfma_f32_16x16x32_bf16 v[58:61], v[166:169], v[198:201], v[58:61]
	s_waitcnt vmcnt(7)
	v_mfma_f32_16x16x32_bf16 v[54:57], v[174:177], v[198:201], v[54:57]
	v_mfma_f32_16x16x32_bf16 v[50:53], v[166:169], v[194:197], v[50:53]
	v_mfma_f32_16x16x32_bf16 v[46:49], v[174:177], v[194:197], v[46:49]
	v_mfma_f32_16x16x32_bf16 v[42:45], v[166:169], v[202:205], v[42:45]
	v_mfma_f32_16x16x32_bf16 v[14:17], v[174:177], v[202:205], v[14:17]
.LBB0_1278:
	ds_read_b128 v[198:201], v241 offset:12288
	ds_read_b128 v[194:197], v241 offset:16384
	ds_read_b128 v[202:205], v241 offset:20480
.LBB0_1280:
	s_lshl_b32 s38, s66, 2
	s_ashr_i32 s39, s38, 31
	s_lshl_b64 s[76:77], s[20:21], 19
	s_lshl_b64 s[38:39], s[38:39], 10
	v_lshl_add_u64 v[4:5], v[214:215], 0, s[76:77]
	v_lshl_add_u64 v[4:5], v[4:5], 0, s[38:39]
	s_waitcnt vmcnt(18)
	v_add_co_u32_e32 v150, vcc, 0x8000, v4
	s_nop 1
	v_addc_co_u32_e32 v151, vcc, 0, v5, vcc
	global_load_dwordx4 v[166:169], v[4:5], off
	global_load_dwordx4 v[174:177], v[150:151], off
	s_waitcnt vmcnt(11) lgkmcnt(2)
	v_mfma_f32_16x16x32_bf16 v[182:185], v[146:149], v[18:21], v[182:185]
	s_waitcnt vmcnt(8)
	v_mfma_f32_16x16x32_bf16 v[162:165], v[170:173], v[18:21], v[162:165]
	s_waitcnt lgkmcnt(1)
	v_mfma_f32_16x16x32_bf16 v[134:137], v[146:149], v[22:25], v[134:137]
	v_mfma_f32_16x16x32_bf16 v[118:121], v[170:173], v[22:25], v[118:121]
	s_waitcnt lgkmcnt(0)
	v_mfma_f32_16x16x32_bf16 v[102:105], v[146:149], v[34:37], v[102:105]
	v_mfma_f32_16x16x32_bf16 v[86:89], v[170:173], v[34:37], v[86:89]
.LBB0_1282:
	s_waitcnt lgkmcnt(1)
	ds_read_b128 v[22:25], v241 offset:28672
	ds_read_b128 v[18:21], v241 offset:24576
	s_waitcnt lgkmcnt(2)
	ds_read_b128 v[34:37], v241 offset:32768
.LBB0_1284:
	global_load_dwordx4 v[186:189], v[4:5], off offset:1024
	s_waitcnt vmcnt(18)
	ds_write_b128 v239, v[106:109]
	s_waitcnt vmcnt(12) lgkmcnt(3)
	v_mfma_f32_16x16x32_bf16 v[82:85], v[146:149], v[198:201], v[82:85]
	s_waitcnt vmcnt(9)
	v_mfma_f32_16x16x32_bf16 v[78:81], v[170:173], v[198:201], v[78:81]
	s_waitcnt lgkmcnt(2)
	v_mfma_f32_16x16x32_bf16 v[74:77], v[146:149], v[194:197], v[74:77]
	v_mfma_f32_16x16x32_bf16 v[70:73], v[170:173], v[194:197], v[70:73]
	s_waitcnt lgkmcnt(1)
	v_mfma_f32_16x16x32_bf16 v[66:69], v[146:149], v[202:205], v[66:69]
	v_mfma_f32_16x16x32_bf16 v[62:65], v[170:173], v[202:205], v[62:65]
.LBB0_1286:
	s_waitcnt lgkmcnt(3)
	ds_read_b128 v[198:201], v242
	s_waitcnt lgkmcnt(3)
	ds_read_b128 v[194:197], v242 offset:4096
	s_waitcnt lgkmcnt(3)
	ds_read_b128 v[202:205], v242 offset:8192
.LBB0_1288:
	global_load_dwordx4 v[158:161], v[4:5], off offset:2048
	s_waitcnt vmcnt(18)
	ds_write_b128 v235, v[94:97] offset:45056
	s_waitcnt vmcnt(13) lgkmcnt(3)
	v_mfma_f32_16x16x32_bf16 v[58:61], v[146:149], v[18:21], v[58:61]
	s_waitcnt vmcnt(10)
	v_mfma_f32_16x16x32_bf16 v[54:57], v[170:173], v[18:21], v[54:57]
	v_mfma_f32_16x16x32_bf16 v[50:53], v[146:149], v[22:25], v[50:53]
	v_mfma_f32_16x16x32_bf16 v[46:49], v[170:173], v[22:25], v[46:49]
	s_waitcnt lgkmcnt(2)
	v_mfma_f32_16x16x32_bf16 v[42:45], v[146:149], v[34:37], v[42:45]
	v_mfma_f32_16x16x32_bf16 v[14:17], v[170:173], v[34:37], v[14:17]
.LBB0_1290:
	s_waitcnt lgkmcnt(3)
	ds_read_b128 v[18:21], v242 offset:12288
	ds_read_b128 v[22:25], v242 offset:16384
	s_waitcnt lgkmcnt(4)
	ds_read_b128 v[34:37], v242 offset:20480
.LBB0_1292:
	v_add_co_u32_e32 v94, vcc, 0x8000, v4
	s_waitcnt vmcnt(17)
	ds_write_b128 v235, v[98:101] offset:53248
	v_addc_co_u32_e32 v95, vcc, 0, v5, vcc
	global_load_dwordx4 v[170:173], v[94:95], off offset:1024
	s_waitcnt vmcnt(13) lgkmcnt(4)
	v_mfma_f32_16x16x32_bf16 v[182:185], v[114:117], v[198:201], v[182:185]
	s_waitcnt vmcnt(10)
	v_mfma_f32_16x16x32_bf16 v[162:165], v[154:157], v[198:201], v[162:165]
	s_waitcnt lgkmcnt(3)
	v_mfma_f32_16x16x32_bf16 v[134:137], v[114:117], v[194:197], v[134:137]
	v_mfma_f32_16x16x32_bf16 v[118:121], v[154:157], v[194:197], v[118:121]
	s_waitcnt lgkmcnt(2)
	v_mfma_f32_16x16x32_bf16 v[102:105], v[114:117], v[202:205], v[102:105]
	v_mfma_f32_16x16x32_bf16 v[86:89], v[154:157], v[202:205], v[86:89]
.LBB0_1294:
	s_waitcnt lgkmcnt(3)
	ds_read_b128 v[194:197], v242 offset:28672
	ds_read_b128 v[198:201], v242 offset:24576
	s_waitcnt lgkmcnt(4)
	ds_read_b128 v[202:205], v242 offset:32768
.LBB0_1296:
	global_load_dwordx4 v[150:153], v[4:5], off offset:3072
	s_waitcnt vmcnt(18)
	ds_write_b128 v235, v[90:93] offset:61440
	s_waitcnt vmcnt(14) lgkmcnt(4)
	v_mfma_f32_16x16x32_bf16 v[82:85], v[114:117], v[18:21], v[82:85]
	s_waitcnt vmcnt(11)
	v_mfma_f32_16x16x32_bf16 v[78:81], v[154:157], v[18:21], v[78:81]
	s_waitcnt lgkmcnt(3)
	v_mfma_f32_16x16x32_bf16 v[74:77], v[114:117], v[22:25], v[74:77]
	v_mfma_f32_16x16x32_bf16 v[70:73], v[154:157], v[22:25], v[70:73]
	s_waitcnt lgkmcnt(2)
	v_mfma_f32_16x16x32_bf16 v[66:69], v[114:117], v[34:37], v[66:69]
	v_mfma_f32_16x16x32_bf16 v[62:65], v[154:157], v[34:37], v[62:65]
.LBB0_1298:
	s_waitcnt lgkmcnt(4)
	ds_read_b128 v[18:21], v243
	s_waitcnt lgkmcnt(4)
	ds_read_b128 v[22:25], v243 offset:4096
	s_waitcnt lgkmcnt(4)
	ds_read_b128 v[34:37], v243 offset:8192
.LBB0_1300:
	v_add_co_u32_e32 v90, vcc, 0x8000, v4
	s_nop 1
	v_addc_co_u32_e32 v91, vcc, 0, v5, vcc
	global_load_dwordx4 v[190:193], v[90:91], off offset:2048
	s_and_saveexec_b64 s[38:39], s[48:49]
	ds_write_b128 v239, v[10:13] offset:32768
	s_or_b64 exec, exec, s[38:39]
	s_waitcnt vmcnt(15) lgkmcnt(2)
	v_mfma_f32_16x16x32_bf16 v[58:61], v[114:117], v[198:201], v[58:61]
	s_waitcnt vmcnt(12)
	v_mfma_f32_16x16x32_bf16 v[54:57], v[154:157], v[198:201], v[54:57]
	v_mfma_f32_16x16x32_bf16 v[50:53], v[114:117], v[194:197], v[50:53]
	v_mfma_f32_16x16x32_bf16 v[46:49], v[154:157], v[194:197], v[46:49]
	s_waitcnt lgkmcnt(1)
	v_mfma_f32_16x16x32_bf16 v[42:45], v[114:117], v[202:205], v[42:45]
	v_mfma_f32_16x16x32_bf16 v[14:17], v[154:157], v[202:205], v[14:17]
.LBB0_1304:
	s_waitcnt lgkmcnt(2)
	ds_read_b128 v[198:201], v243 offset:12288
	ds_read_b128 v[194:197], v243 offset:16384
	s_waitcnt lgkmcnt(3)
	ds_read_b128 v[202:205], v243 offset:20480
.LBB0_1306:
	v_add_co_u32_e32 v4, vcc, 0x8000, v4
	s_nop 1
	v_addc_co_u32_e32 v5, vcc, 0, v5, vcc
	global_load_dwordx4 v[178:181], v[4:5], off offset:3072
	s_waitcnt vmcnt(14) lgkmcnt(2)
	v_mfma_f32_16x16x32_bf16 v[182:185], v[110:113], v[18:21], v[182:185]
	s_waitcnt vmcnt(12)
	v_mfma_f32_16x16x32_bf16 v[162:165], v[138:141], v[18:21], v[162:165]
	s_waitcnt lgkmcnt(1)
	v_mfma_f32_16x16x32_bf16 v[134:137], v[110:113], v[22:25], v[134:137]
	v_mfma_f32_16x16x32_bf16 v[118:121], v[138:141], v[22:25], v[118:121]
	s_waitcnt lgkmcnt(0)
	v_mfma_f32_16x16x32_bf16 v[102:105], v[110:113], v[34:37], v[102:105]
	v_mfma_f32_16x16x32_bf16 v[86:89], v[138:141], v[34:37], v[86:89]
.LBB0_1308:
	s_waitcnt lgkmcnt(1)
	ds_read_b128 v[22:25], v243 offset:28672
	ds_read_b128 v[18:21], v243 offset:24576
	s_waitcnt lgkmcnt(2)
	ds_read_b128 v[34:37], v243 offset:32768
.LBB0_1310:
	s_waitcnt vmcnt(14) lgkmcnt(2)
	v_mfma_f32_16x16x32_bf16 v[82:85], v[110:113], v[198:201], v[82:85]
	s_waitcnt vmcnt(12)
	v_mfma_f32_16x16x32_bf16 v[78:81], v[138:141], v[198:201], v[78:81]
	s_waitcnt lgkmcnt(1)
	v_mfma_f32_16x16x32_bf16 v[74:77], v[110:113], v[194:197], v[74:77]
	v_mfma_f32_16x16x32_bf16 v[70:73], v[138:141], v[194:197], v[70:73]
	s_waitcnt lgkmcnt(0)
	v_mfma_f32_16x16x32_bf16 v[66:69], v[110:113], v[202:205], v[66:69]
	v_mfma_f32_16x16x32_bf16 v[62:65], v[138:141], v[202:205], v[62:65]
.LBB0_1312:
	s_waitcnt vmcnt(14) lgkmcnt(1)
	v_mfma_f32_16x16x32_bf16 v[58:61], v[110:113], v[18:21], v[58:61]
	s_waitcnt vmcnt(12)
	v_mfma_f32_16x16x32_bf16 v[54:57], v[138:141], v[18:21], v[54:57]
	v_mfma_f32_16x16x32_bf16 v[50:53], v[110:113], v[22:25], v[50:53]
	v_mfma_f32_16x16x32_bf16 v[46:49], v[138:141], v[22:25], v[46:49]
	s_waitcnt lgkmcnt(0)
	v_mfma_f32_16x16x32_bf16 v[42:45], v[110:113], v[34:37], v[42:45]
	v_mfma_f32_16x16x32_bf16 v[14:17], v[138:141], v[34:37], v[14:17]
.LBB0_1314:
	s_add_i32 s75, s75, 1
	s_cmp_lg_u32 s75, 8
	s_cbranch_scc1 .LBB0_1316
	v_mov_b32_e32 v3, v237
	v_mov_b32_e32 v5, v236
	s_lshl_b32 s12, s74, 7
	s_add_i32 s12, s12, s65
	v_lshl_add_u32 v4, v5, 2, 0
	v_add_u32_e32 v4, 0x25500, v4
	v_lshl_add_u32 v98, v3, 2, s12
	ds_read2_b32 v[96:97], v4 offset1:16
	ds_read2_b32 v[94:95], v4 offset0:32 offset1:48
	ds_read2_b32 v[92:93], v4 offset0:64 offset1:80
	ds_read2_b32 v[90:91], v4 offset0:96 offset1:112
	ds_read_b32 v4, v4 offset:512
	v_lshrrev_b32_e32 v99, 7, v98
	v_lshrrev_b32_e32 v98, 3, v98
	v_mul_lo_u32 v108, v99, s80
	v_lshlrev_b32_e32 v109, 8, v5
	v_xor_b32_e32 v5, v98, v5
	s_waitcnt lgkmcnt(4)
	v_pk_mul_f32 v[98:99], v[182:183], v[96:97] op_sel_hi:[1,0]
	v_lshlrev_b32_e32 v5, 4, v5
	v_mul_f32_e32 v100, 0xbfb8aa3b, v98
	v_mul_f32_e32 v101, 0xbfb8aa3b, v99
	v_exp_f32_e32 v100, v100
	v_exp_f32_e32 v101, v101
	v_lshlrev_b32_e32 v3, 3, v3
	s_add_i32 s12, 0, 0x12000
	v_add_f32_e32 v100, 1.0, v100
	v_add_f32_e32 v101, 1.0, v101
	v_rcp_f32_e32 v100, v100
	v_rcp_f32_e32 v101, v101
	v_and_b32_e32 v5, 0xf0, v5
	v_and_b32_e32 v3, 8, v3
	s_waitcnt lgkmcnt(3)
	v_pk_mul_f32 v[86:87], v[86:87], v[94:95] op_sel_hi:[1,0]
	v_pk_mul_f32 v[98:99], v[98:99], v[100:101]
	v_pk_mul_f32 v[100:101], v[162:163], v[96:97] op_sel_hi:[1,0]
	v_pk_mul_f32 v[88:89], v[88:89], v[94:95] op_sel_hi:[1,0]
	v_pk_mul_f32 v[98:99], v[100:101], v[98:99]
	v_pk_mul_f32 v[100:101], v[184:185], v[96:97] op_sel_hi:[1,0]
	v_cvt_pk_bf16_f32 v98, v98, v99
	v_mul_f32_e32 v106, 0xbfb8aa3b, v100
	v_mul_f32_e32 v107, 0xbfb8aa3b, v101
	v_exp_f32_e32 v106, v106
	v_exp_f32_e32 v107, v107
	s_waitcnt lgkmcnt(2)
	v_pk_mul_f32 v[74:75], v[74:75], v[92:93] op_sel_hi:[1,0]
	v_pk_mul_f32 v[70:71], v[70:71], v[92:93] op_sel_hi:[1,0]
	v_add_f32_e32 v106, 1.0, v106
	v_add_f32_e32 v107, 1.0, v107
	v_rcp_f32_e32 v106, v106
	v_rcp_f32_e32 v107, v107
	v_pk_mul_f32 v[72:73], v[72:73], v[92:93] op_sel_hi:[1,0]
	s_waitcnt lgkmcnt(1)
	v_pk_mul_f32 v[58:59], v[58:59], v[90:91] op_sel_hi:[1,0]
	v_pk_mul_f32 v[54:55], v[54:55], v[90:91] op_sel_hi:[1,0]
	v_pk_mul_f32 v[100:101], v[100:101], v[106:107]
	v_pk_mul_f32 v[106:107], v[164:165], v[96:97] op_sel_hi:[1,0]
	v_add3_u32 v96, s12, v108, v109
	v_pk_mul_f32 v[100:101], v[106:107], v[100:101]
	v_add3_u32 v96, v96, v5, v3
	v_cvt_pk_bf16_f32 v99, v100, v101
	ds_write_b64 v96, v[98:99]
	v_mov_b32_e32 v96, v97
	v_pk_mul_f32 v[98:99], v[134:135], v[96:97] op_sel_hi:[1,0]
	v_pk_mul_f32 v[56:57], v[56:57], v[90:91] op_sel_hi:[1,0]
	v_mul_f32_e32 v97, 0xbfb8aa3b, v98
	v_exp_f32_e32 v97, v97
	s_add_i32 s74, s74, 1
	s_mov_b32 s75, 0
	v_add_f32_e32 v97, 1.0, v97
	v_rcp_f32_e32 v100, v97
	v_mul_f32_e32 v97, 0xbfb8aa3b, v99
	v_exp_f32_e32 v97, v97
	s_nop 0
	v_add_f32_e32 v97, 1.0, v97
	v_rcp_f32_e32 v101, v97
	s_nop 0
	v_pk_mul_f32 v[98:99], v[98:99], v[100:101]
	v_pk_mul_f32 v[100:101], v[118:119], v[96:97] op_sel_hi:[1,0]
	s_nop 0
	v_pk_mul_f32 v[98:99], v[100:101], v[98:99]
	v_pk_mul_f32 v[100:101], v[136:137], v[96:97] op_sel_hi:[1,0]
	v_cvt_pk_bf16_f32 v98, v98, v99
	v_mul_f32_e32 v97, 0xbfb8aa3b, v100
	v_exp_f32_e32 v97, v97
	s_nop 0
	v_add_f32_e32 v97, 1.0, v97
	v_rcp_f32_e32 v106, v97
	v_mul_f32_e32 v97, 0xbfb8aa3b, v101
	v_exp_f32_e32 v97, v97
	s_nop 0
	v_add_f32_e32 v97, 1.0, v97
	v_rcp_f32_e32 v107, v97
	v_pk_mul_f32 v[96:97], v[120:121], v[96:97] op_sel_hi:[1,0]
	v_pk_mul_f32 v[100:101], v[100:101], v[106:107]
	s_nop 0
	v_pk_mul_f32 v[96:97], v[96:97], v[100:101]
	s_nop 0
	v_cvt_pk_bf16_f32 v99, v96, v97
	v_add3_u32 v96, 0, v108, v109
	v_add3_u32 v3, v96, v5, v3
	v_add_u32_e32 v5, 0x13000, v3
	v_pk_mul_f32 v[96:97], v[102:103], v[94:95] op_sel_hi:[1,0]
	ds_write_b64 v5, v[98:99]
	v_mul_f32_e32 v5, 0xbfb8aa3b, v96
	v_exp_f32_e32 v5, v5
	s_nop 0
	v_add_f32_e32 v5, 1.0, v5
	v_rcp_f32_e32 v98, v5
	v_mul_f32_e32 v5, 0xbfb8aa3b, v97
	v_exp_f32_e32 v5, v5
	s_nop 0
	v_add_f32_e32 v5, 1.0, v5
	v_rcp_f32_e32 v99, v5
	s_nop 0
	v_pk_mul_f32 v[96:97], v[96:97], v[98:99]
	s_nop 0
	v_pk_mul_f32 v[86:87], v[86:87], v[96:97]
	v_pk_mul_f32 v[96:97], v[104:105], v[94:95] op_sel_hi:[1,0]
	v_cvt_pk_bf16_f32 v86, v86, v87
	v_mul_f32_e32 v5, 0xbfb8aa3b, v96
	v_exp_f32_e32 v5, v5
	s_nop 0
	v_add_f32_e32 v5, 1.0, v5
	v_rcp_f32_e32 v98, v5
	v_mul_f32_e32 v5, 0xbfb8aa3b, v97
	v_exp_f32_e32 v5, v5
	s_nop 0
	v_add_f32_e32 v5, 1.0, v5
	v_rcp_f32_e32 v99, v5
	v_add_u32_e32 v5, 0x14000, v3
	v_pk_mul_f32 v[96:97], v[96:97], v[98:99]
	s_nop 0
	v_pk_mul_f32 v[88:89], v[88:89], v[96:97]
	s_nop 0
	v_cvt_pk_bf16_f32 v87, v88, v89
	ds_write_b64 v5, v[86:87]
	v_mov_b32_e32 v86, v95
	v_pk_mul_f32 v[82:83], v[82:83], v[86:87] op_sel_hi:[1,0]
	v_pk_mul_f32 v[78:79], v[78:79], v[86:87] op_sel_hi:[1,0]
	v_mul_f32_e32 v5, 0xbfb8aa3b, v82
	v_exp_f32_e32 v5, v5
	v_pk_mul_f32 v[80:81], v[80:81], v[86:87] op_sel_hi:[1,0]
	v_add_f32_e32 v5, 1.0, v5
	v_rcp_f32_e32 v88, v5
	v_mul_f32_e32 v5, 0xbfb8aa3b, v83
	v_exp_f32_e32 v5, v5
	s_nop 0
	v_add_f32_e32 v5, 1.0, v5
	v_rcp_f32_e32 v89, v5
	s_nop 0
	v_pk_mul_f32 v[82:83], v[82:83], v[88:89]
	s_nop 0
	v_pk_mul_f32 v[78:79], v[78:79], v[82:83]
	v_pk_mul_f32 v[82:83], v[84:85], v[86:87] op_sel_hi:[1,0]
	v_cvt_pk_bf16_f32 v78, v78, v79
	v_mul_f32_e32 v5, 0xbfb8aa3b, v82
	v_exp_f32_e32 v5, v5
	s_nop 0
	v_add_f32_e32 v5, 1.0, v5
	v_rcp_f32_e32 v84, v5
	v_mul_f32_e32 v5, 0xbfb8aa3b, v83
	v_exp_f32_e32 v5, v5
	s_nop 0
	v_add_f32_e32 v5, 1.0, v5
	v_rcp_f32_e32 v85, v5
	v_add_u32_e32 v5, 0x15000, v3
	v_pk_mul_f32 v[82:83], v[82:83], v[84:85]
	s_nop 0
	v_pk_mul_f32 v[80:81], v[80:81], v[82:83]
	s_nop 0
	v_cvt_pk_bf16_f32 v79, v80, v81
	ds_write_b64 v5, v[78:79]
	v_mul_f32_e32 v5, 0xbfb8aa3b, v74
	v_exp_f32_e32 v5, v5
	s_nop 0
	v_add_f32_e32 v5, 1.0, v5
	v_rcp_f32_e32 v78, v5
	v_mul_f32_e32 v5, 0xbfb8aa3b, v75
	v_exp_f32_e32 v5, v5
	s_nop 0
	v_add_f32_e32 v5, 1.0, v5
	v_rcp_f32_e32 v79, v5
	s_nop 0
	v_pk_mul_f32 v[74:75], v[74:75], v[78:79]
	s_nop 0
	v_pk_mul_f32 v[70:71], v[70:71], v[74:75]
	v_pk_mul_f32 v[74:75], v[76:77], v[92:93] op_sel_hi:[1,0]
	v_cvt_pk_bf16_f32 v70, v70, v71
	v_mul_f32_e32 v5, 0xbfb8aa3b, v74
	v_exp_f32_e32 v5, v5
	s_nop 0
	v_add_f32_e32 v5, 1.0, v5
	v_rcp_f32_e32 v76, v5
	v_mul_f32_e32 v5, 0xbfb8aa3b, v75
	v_exp_f32_e32 v5, v5
	s_nop 0
	v_add_f32_e32 v5, 1.0, v5
	v_rcp_f32_e32 v77, v5
	v_add_u32_e32 v5, 0x16000, v3
	v_pk_mul_f32 v[74:75], v[74:75], v[76:77]
	s_nop 0
	v_pk_mul_f32 v[72:73], v[72:73], v[74:75]
	s_nop 0
	v_cvt_pk_bf16_f32 v71, v72, v73
	ds_write_b64 v5, v[70:71]
	v_mov_b32_e32 v70, v93
	v_pk_mul_f32 v[66:67], v[66:67], v[70:71] op_sel_hi:[1,0]
	v_pk_mul_f32 v[62:63], v[62:63], v[70:71] op_sel_hi:[1,0]
	v_mul_f32_e32 v5, 0xbfb8aa3b, v66
	v_exp_f32_e32 v5, v5
	v_pk_mul_f32 v[64:65], v[64:65], v[70:71] op_sel_hi:[1,0]
	v_add_f32_e32 v5, 1.0, v5
	v_rcp_f32_e32 v72, v5
	v_mul_f32_e32 v5, 0xbfb8aa3b, v67
	v_exp_f32_e32 v5, v5
	s_nop 0
	v_add_f32_e32 v5, 1.0, v5
	v_rcp_f32_e32 v73, v5
	s_nop 0
	v_pk_mul_f32 v[66:67], v[66:67], v[72:73]
	s_nop 0
	v_pk_mul_f32 v[62:63], v[62:63], v[66:67]
	v_pk_mul_f32 v[66:67], v[68:69], v[70:71] op_sel_hi:[1,0]
	v_cvt_pk_bf16_f32 v62, v62, v63
	v_mul_f32_e32 v5, 0xbfb8aa3b, v66
	v_exp_f32_e32 v5, v5
	s_nop 0
	v_add_f32_e32 v5, 1.0, v5
	v_rcp_f32_e32 v68, v5
	v_mul_f32_e32 v5, 0xbfb8aa3b, v67
	v_exp_f32_e32 v5, v5
	s_nop 0
	v_add_f32_e32 v5, 1.0, v5
	v_rcp_f32_e32 v69, v5
	v_add_u32_e32 v5, 0x17000, v3
	v_pk_mul_f32 v[66:67], v[66:67], v[68:69]
	s_nop 0
	v_pk_mul_f32 v[64:65], v[64:65], v[66:67]
	s_nop 0
	v_cvt_pk_bf16_f32 v63, v64, v65
	ds_write_b64 v5, v[62:63]
	v_mul_f32_e32 v5, 0xbfb8aa3b, v58
	v_exp_f32_e32 v5, v5
	s_nop 0
	v_add_f32_e32 v5, 1.0, v5
	v_rcp_f32_e32 v62, v5
	v_mul_f32_e32 v5, 0xbfb8aa3b, v59
	v_exp_f32_e32 v5, v5
	s_nop 0
	v_add_f32_e32 v5, 1.0, v5
	v_rcp_f32_e32 v63, v5
	s_nop 0
	v_pk_mul_f32 v[58:59], v[58:59], v[62:63]
	s_nop 0
	v_pk_mul_f32 v[54:55], v[54:55], v[58:59]
	v_pk_mul_f32 v[58:59], v[60:61], v[90:91] op_sel_hi:[1,0]
	v_cvt_pk_bf16_f32 v54, v54, v55
	v_mul_f32_e32 v5, 0xbfb8aa3b, v58
	v_exp_f32_e32 v5, v5
	s_nop 0
	v_add_f32_e32 v5, 1.0, v5
	v_rcp_f32_e32 v60, v5
	v_mul_f32_e32 v5, 0xbfb8aa3b, v59
	v_exp_f32_e32 v5, v5
	s_nop 0
	v_add_f32_e32 v5, 1.0, v5
	v_rcp_f32_e32 v61, v5
	v_add_u32_e32 v5, 0x18000, v3
	v_pk_mul_f32 v[58:59], v[58:59], v[60:61]
	s_nop 0
	v_pk_mul_f32 v[56:57], v[56:57], v[58:59]
	s_nop 0
	v_cvt_pk_bf16_f32 v55, v56, v57
	ds_write_b64 v5, v[54:55]
	v_mov_b32_e32 v54, v91
	v_pk_mul_f32 v[50:51], v[50:51], v[54:55] op_sel_hi:[1,0]
	v_pk_mul_f32 v[46:47], v[46:47], v[54:55] op_sel_hi:[1,0]
	v_mul_f32_e32 v5, 0xbfb8aa3b, v50
	v_exp_f32_e32 v5, v5
	v_pk_mul_f32 v[48:49], v[48:49], v[54:55] op_sel_hi:[1,0]
	v_add_f32_e32 v5, 1.0, v5
	v_rcp_f32_e32 v56, v5
	v_mul_f32_e32 v5, 0xbfb8aa3b, v51
	v_exp_f32_e32 v5, v5
	s_nop 0
	v_add_f32_e32 v5, 1.0, v5
	v_rcp_f32_e32 v57, v5
	s_nop 0
	v_pk_mul_f32 v[50:51], v[50:51], v[56:57]
	s_nop 0
	v_pk_mul_f32 v[46:47], v[46:47], v[50:51]
	v_pk_mul_f32 v[50:51], v[52:53], v[54:55] op_sel_hi:[1,0]
	v_cvt_pk_bf16_f32 v46, v46, v47
	v_mul_f32_e32 v5, 0xbfb8aa3b, v50
	v_exp_f32_e32 v5, v5
	s_nop 0
	v_add_f32_e32 v5, 1.0, v5
	v_rcp_f32_e32 v52, v5
	v_mul_f32_e32 v5, 0xbfb8aa3b, v51
	v_exp_f32_e32 v5, v5
	s_nop 0
	v_add_f32_e32 v5, 1.0, v5
	v_rcp_f32_e32 v53, v5
	v_add_u32_e32 v5, 0x19000, v3
	s_waitcnt lgkmcnt(7)
	v_pk_mul_f32 v[42:43], v[42:43], v[4:5] op_sel_hi:[1,0]
	v_add_u32_e32 v3, 0x1a000, v3
	v_pk_mul_f32 v[50:51], v[50:51], v[52:53]
	s_nop 0
	v_pk_mul_f32 v[48:49], v[48:49], v[50:51]
	s_nop 0
	v_cvt_pk_bf16_f32 v47, v48, v49
	ds_write_b64 v5, v[46:47]
	v_mul_f32_e32 v5, 0xbfb8aa3b, v42
	v_exp_f32_e32 v5, v5
	s_nop 0
	v_add_f32_e32 v5, 1.0, v5
	v_rcp_f32_e32 v46, v5
	v_mul_f32_e32 v5, 0xbfb8aa3b, v43
	v_exp_f32_e32 v5, v5
	s_nop 0
	v_add_f32_e32 v5, 1.0, v5
	v_rcp_f32_e32 v47, v5
	v_pk_mul_f32 v[14:15], v[14:15], v[4:5] op_sel_hi:[1,0]
	v_pk_mul_f32 v[42:43], v[42:43], v[46:47]
	s_nop 0
	v_pk_mul_f32 v[14:15], v[14:15], v[42:43]
	v_pk_mul_f32 v[42:43], v[44:45], v[4:5] op_sel_hi:[1,0]
	v_cvt_pk_bf16_f32 v14, v14, v15
	v_mul_f32_e32 v5, 0xbfb8aa3b, v42
	v_exp_f32_e32 v5, v5
	s_nop 0
	v_add_f32_e32 v5, 1.0, v5
	v_rcp_f32_e32 v44, v5
	v_mul_f32_e32 v5, 0xbfb8aa3b, v43
	v_exp_f32_e32 v5, v5
	s_nop 0
	v_add_f32_e32 v5, 1.0, v5
	v_rcp_f32_e32 v45, v5
	v_pk_mul_f32 v[4:5], v[16:17], v[4:5] op_sel_hi:[1,0]
	v_pk_mul_f32 v[42:43], v[42:43], v[44:45]
	s_nop 0
	v_pk_mul_f32 v[4:5], v[4:5], v[42:43]
	s_nop 0
	v_cvt_pk_bf16_f32 v15, v4, v5
	v_mov_b32_e32 v4, v2
	v_mov_b32_e32 v5, v2
	ds_write_b64 v3, v[14:15]
	v_mov_b32_e32 v3, v2
	v_mov_b64_e32 v[16:17], v[4:5]
	v_mov_b64_e32 v[44:45], v[4:5]
	v_mov_b64_e32 v[48:49], v[4:5]
	v_mov_b64_e32 v[52:53], v[4:5]
	v_mov_b64_e32 v[56:57], v[4:5]
	v_mov_b64_e32 v[60:61], v[4:5]
	v_mov_b64_e32 v[64:65], v[4:5]
	v_mov_b64_e32 v[68:69], v[4:5]
	v_mov_b64_e32 v[72:73], v[4:5]
	v_mov_b64_e32 v[76:77], v[4:5]
	v_mov_b64_e32 v[80:81], v[4:5]
	v_mov_b64_e32 v[84:85], v[4:5]
	v_mov_b64_e32 v[88:89], v[4:5]
	v_mov_b64_e32 v[104:105], v[4:5]
	v_mov_b64_e32 v[120:121], v[4:5]
	v_mov_b64_e32 v[136:137], v[4:5]
	v_mov_b64_e32 v[164:165], v[4:5]
	v_mov_b64_e32 v[184:185], v[4:5]
	v_mov_b64_e32 v[14:15], v[2:3]
	v_mov_b64_e32 v[42:43], v[2:3]
	v_mov_b64_e32 v[46:47], v[2:3]
	v_mov_b64_e32 v[50:51], v[2:3]
	v_mov_b64_e32 v[54:55], v[2:3]
	v_mov_b64_e32 v[58:59], v[2:3]
	v_mov_b64_e32 v[62:63], v[2:3]
	v_mov_b64_e32 v[66:67], v[2:3]
	v_mov_b64_e32 v[70:71], v[2:3]
	v_mov_b64_e32 v[74:75], v[2:3]
	v_mov_b64_e32 v[78:79], v[2:3]
	v_mov_b64_e32 v[82:83], v[2:3]
	v_mov_b64_e32 v[86:87], v[2:3]
	v_mov_b64_e32 v[102:103], v[2:3]
	v_mov_b64_e32 v[118:119], v[2:3]
	v_mov_b64_e32 v[134:135], v[2:3]
	v_mov_b64_e32 v[162:163], v[2:3]
	v_mov_b64_e32 v[182:183], v[2:3]
.LBB0_1316:
	s_waitcnt lgkmcnt(0)
	s_barrier
	ds_read_b128 v[198:201], v238 offset:36864
	ds_read_b128 v[194:197], v238 offset:40960
	ds_read_b128 v[202:205], v238 offset:45056
	ds_read_b128 v[26:29], v238 offset:49152
	ds_read_b128 v[30:33], v238 offset:53248
	ds_read_b128 v[38:41], v238 offset:57344
.LBB0_1318:
	s_add_i32 s12, s67, 1
	s_cmp_lg_u32 s12, 8
	s_cselect_b32 s67, s12, 0
	v_lshl_or_b32 v4, s67, 7, v234
	v_ashrrev_i32_e32 v5, 31, v4
	ds_read2_b32 v[92:93], v233 offset1:32
	v_lshlrev_b64 v[90:91], 1, v[4:5]
	s_waitcnt lgkmcnt(0)
	v_ashrrev_i32_e32 v95, 31, v92
	v_mov_b32_e32 v94, v92
	v_ashrrev_i32_e32 v97, 31, v93
	v_mov_b32_e32 v96, v93
	v_lshlrev_b64 v[92:93], 11, v[94:95]
	v_lshlrev_b64 v[94:95], 11, v[96:97]
	v_lshl_add_u64 v[92:93], s[6:7], 0, v[92:93]
	v_lshl_add_u64 v[94:95], s[6:7], 0, v[94:95]
	v_lshl_add_u64 v[92:93], v[92:93], 0, v[90:91]
	v_lshl_add_u64 v[94:95], v[94:95], 0, v[90:91]
	global_load_dwordx4 v[106:109], v[92:93], off
	s_nop 0
	global_load_dwordx4 v[94:97], v[94:95], off
	s_waitcnt vmcnt(9)
	v_mfma_f32_16x16x32_bf16 v[182:185], v[166:169], v[198:201], v[182:185]
	s_waitcnt vmcnt(8)
	v_mfma_f32_16x16x32_bf16 v[162:165], v[174:177], v[198:201], v[162:165]
	v_mfma_f32_16x16x32_bf16 v[134:137], v[166:169], v[194:197], v[134:137]
	v_mfma_f32_16x16x32_bf16 v[118:121], v[174:177], v[194:197], v[118:121]
	v_mfma_f32_16x16x32_bf16 v[102:105], v[166:169], v[202:205], v[102:105]
	v_mfma_f32_16x16x32_bf16 v[86:89], v[174:177], v[202:205], v[86:89]
.LBB0_1320:
	ds_read_b128 v[194:197], v240 offset:28672
	ds_read_b128 v[198:201], v238 offset:61440
	ds_read_b128 v[202:205], v240 offset:32768
.LBB0_1322:
	ds_read2_b32 v[92:93], v233 offset0:64 offset1:96
	s_waitcnt lgkmcnt(0)
	v_ashrrev_i32_e32 v99, 31, v92
	v_mov_b32_e32 v98, v92
	v_ashrrev_i32_e32 v101, 31, v93
	v_mov_b32_e32 v100, v93
	v_lshlrev_b64 v[92:93], 11, v[98:99]
	v_lshlrev_b64 v[98:99], 11, v[100:101]
	v_lshl_add_u64 v[92:93], s[6:7], 0, v[92:93]
	v_lshl_add_u64 v[98:99], s[6:7], 0, v[98:99]
	v_lshl_add_u64 v[92:93], v[92:93], 0, v[90:91]
	v_lshl_add_u64 v[90:91], v[98:99], 0, v[90:91]
	global_load_dwordx4 v[98:101], v[92:93], off
	s_nop 0
	global_load_dwordx4 v[90:93], v[90:91], off
	s_waitcnt vmcnt(11)
	v_mfma_f32_16x16x32_bf16 v[82:85], v[166:169], v[26:29], v[82:85]
	s_waitcnt vmcnt(10)
	v_mfma_f32_16x16x32_bf16 v[78:81], v[174:177], v[26:29], v[78:81]
	v_mfma_f32_16x16x32_bf16 v[74:77], v[166:169], v[30:33], v[74:77]
	v_mfma_f32_16x16x32_bf16 v[70:73], v[174:177], v[30:33], v[70:73]
	v_mfma_f32_16x16x32_bf16 v[66:69], v[166:169], v[38:41], v[66:69]
	v_mfma_f32_16x16x32_bf16 v[62:65], v[174:177], v[38:41], v[62:65]
.LBB0_1324:
	ds_read_b128 v[26:29], v241 offset:36864
	ds_read_b128 v[30:33], v241 offset:40960
	ds_read_b128 v[38:41], v241 offset:45056
.LBB0_1326:
	s_and_saveexec_b64 s[38:39], s[48:49]
	s_cbranch_execz .LBB0_1328
	ds_read_b32 v10, v233 offset:512
	s_waitcnt lgkmcnt(0)
	v_ashrrev_i32_e32 v11, 31, v10
	v_lshlrev_b64 v[10:11], 11, v[10:11]
	v_lshl_add_u64 v[10:11], s[6:7], 0, v[10:11]
	v_lshl_add_u64 v[4:5], v[4:5], 1, v[10:11]
	global_load_dwordx4 v[10:13], v[4:5], off
.LBB0_1328:
	s_or_b64 exec, exec, s[38:39]
	s_waitcnt vmcnt(11)
	v_mfma_f32_16x16x32_bf16 v[58:61], v[166:169], v[198:201], v[58:61]
	s_waitcnt vmcnt(10)
	v_mfma_f32_16x16x32_bf16 v[54:57], v[174:177], v[198:201], v[54:57]
	v_mfma_f32_16x16x32_bf16 v[50:53], v[166:169], v[194:197], v[50:53]
	v_mfma_f32_16x16x32_bf16 v[46:49], v[174:177], v[194:197], v[46:49]
	v_mfma_f32_16x16x32_bf16 v[42:45], v[166:169], v[202:205], v[42:45]
	v_mfma_f32_16x16x32_bf16 v[14:17], v[174:177], v[202:205], v[14:17]
.LBB0_1330:
	ds_read_b128 v[198:201], v241 offset:49152
	ds_read_b128 v[194:197], v241 offset:53248
	ds_read_b128 v[202:205], v241 offset:57344
.LBB0_1332:
	s_add_i32 s12, s66, 1
	s_cmp_gt_i32 s20, 0
	s_cselect_b32 s38, s66, 0
	s_cmp_lt_i32 s66, 7
	s_cselect_b32 s66, s12, s38
	s_cselect_b32 s20, s20, 1
	s_lshl_b32 s38, s66, 2
	s_ashr_i32 s39, s38, 31
	s_lshl_b64 s[76:77], s[20:21], 19
	s_lshl_b64 s[38:39], s[38:39], 10
	v_lshl_add_u64 v[4:5], v[214:215], 0, s[76:77]
	v_lshl_add_u64 v[4:5], v[4:5], 0, s[38:39]
	s_waitcnt vmcnt(18)
	v_add_co_u32_e32 v110, vcc, 0x8000, v4
	s_nop 1
	v_addc_co_u32_e32 v111, vcc, 0, v5, vcc
	global_load_dwordx4 v[166:169], v[4:5], off
	global_load_dwordx4 v[174:177], v[110:111], off
	s_waitcnt vmcnt(11) lgkmcnt(2)
	v_mfma_f32_16x16x32_bf16 v[182:185], v[186:189], v[26:29], v[182:185]
	s_waitcnt vmcnt(9)
	v_mfma_f32_16x16x32_bf16 v[162:165], v[170:173], v[26:29], v[162:165]
	s_waitcnt lgkmcnt(1)
	v_mfma_f32_16x16x32_bf16 v[134:137], v[186:189], v[30:33], v[134:137]
	v_mfma_f32_16x16x32_bf16 v[118:121], v[170:173], v[30:33], v[118:121]
	s_waitcnt lgkmcnt(0)
	v_mfma_f32_16x16x32_bf16 v[102:105], v[186:189], v[38:41], v[102:105]
	v_mfma_f32_16x16x32_bf16 v[86:89], v[170:173], v[38:41], v[86:89]
.LBB0_1334:
	s_waitcnt lgkmcnt(1)
	ds_read_b128 v[30:33], v244 offset:28672
	ds_read_b128 v[26:29], v241 offset:61440
	s_waitcnt lgkmcnt(2)
	ds_read_b128 v[38:41], v244 offset:32768
.LBB0_1336:
	global_load_dwordx4 v[146:149], v[4:5], off offset:1024
	s_waitcnt vmcnt(18)
	ds_write_b128 v235, v[142:145]
	s_waitcnt vmcnt(12) lgkmcnt(3)
	v_mfma_f32_16x16x32_bf16 v[82:85], v[186:189], v[198:201], v[82:85]
	s_waitcnt vmcnt(10)
	v_mfma_f32_16x16x32_bf16 v[78:81], v[170:173], v[198:201], v[78:81]
	s_waitcnt lgkmcnt(2)
	v_mfma_f32_16x16x32_bf16 v[74:77], v[186:189], v[194:197], v[74:77]
	v_mfma_f32_16x16x32_bf16 v[70:73], v[170:173], v[194:197], v[70:73]
	s_waitcnt lgkmcnt(1)
	v_mfma_f32_16x16x32_bf16 v[66:69], v[186:189], v[202:205], v[66:69]
	v_mfma_f32_16x16x32_bf16 v[62:65], v[170:173], v[202:205], v[62:65]
.LBB0_1338:
	s_waitcnt lgkmcnt(3)
	ds_read_b128 v[198:201], v242 offset:36864
	s_waitcnt lgkmcnt(3)
	ds_read_b128 v[194:197], v242 offset:40960
	s_waitcnt lgkmcnt(3)
	ds_read_b128 v[202:205], v242 offset:45056
.LBB0_1340:
	global_load_dwordx4 v[114:117], v[4:5], off offset:2048
	s_waitcnt vmcnt(18)
	ds_write_b128 v235, v[126:129] offset:8192
	s_waitcnt vmcnt(13) lgkmcnt(3)
	v_mfma_f32_16x16x32_bf16 v[58:61], v[186:189], v[26:29], v[58:61]
	s_waitcnt vmcnt(11)
	v_mfma_f32_16x16x32_bf16 v[54:57], v[170:173], v[26:29], v[54:57]
	v_mfma_f32_16x16x32_bf16 v[50:53], v[186:189], v[30:33], v[50:53]
	v_mfma_f32_16x16x32_bf16 v[46:49], v[170:173], v[30:33], v[46:49]
	s_waitcnt lgkmcnt(2)
	v_mfma_f32_16x16x32_bf16 v[42:45], v[186:189], v[38:41], v[42:45]
	v_mfma_f32_16x16x32_bf16 v[14:17], v[170:173], v[38:41], v[14:17]
.LBB0_1342:
	s_waitcnt lgkmcnt(3)
	ds_read_b128 v[26:29], v242 offset:49152
	ds_read_b128 v[30:33], v242 offset:53248
	s_waitcnt lgkmcnt(4)
	ds_read_b128 v[38:41], v242 offset:57344
.LBB0_1344:
	v_add_co_u32_e32 v110, vcc, 0x8000, v4
	s_waitcnt vmcnt(17)
	ds_write_b128 v235, v[130:133] offset:16384
	v_addc_co_u32_e32 v111, vcc, 0, v5, vcc
	global_load_dwordx4 v[170:173], v[110:111], off offset:1024
	s_waitcnt vmcnt(13) lgkmcnt(4)
	v_mfma_f32_16x16x32_bf16 v[182:185], v[158:161], v[198:201], v[182:185]
	s_waitcnt vmcnt(10)
	v_mfma_f32_16x16x32_bf16 v[162:165], v[190:193], v[198:201], v[162:165]
	s_waitcnt lgkmcnt(3)
	v_mfma_f32_16x16x32_bf16 v[134:137], v[158:161], v[194:197], v[134:137]
	v_mfma_f32_16x16x32_bf16 v[118:121], v[190:193], v[194:197], v[118:121]
	s_waitcnt lgkmcnt(2)
	v_mfma_f32_16x16x32_bf16 v[102:105], v[158:161], v[202:205], v[102:105]
	v_mfma_f32_16x16x32_bf16 v[86:89], v[190:193], v[202:205], v[86:89]
.LBB0_1346:
	s_waitcnt lgkmcnt(3)
	ds_read_b128 v[194:197], v245 offset:28672
	ds_read_b128 v[198:201], v242 offset:61440
	s_waitcnt lgkmcnt(4)
	ds_read_b128 v[202:205], v245 offset:32768
.LBB0_1348:
	global_load_dwordx4 v[110:113], v[4:5], off offset:3072
	s_waitcnt vmcnt(18)
	ds_write_b128 v235, v[122:125] offset:24576
	s_waitcnt vmcnt(14) lgkmcnt(4)
	v_mfma_f32_16x16x32_bf16 v[82:85], v[158:161], v[26:29], v[82:85]
	s_waitcnt vmcnt(11)
	v_mfma_f32_16x16x32_bf16 v[78:81], v[190:193], v[26:29], v[78:81]
	s_waitcnt lgkmcnt(3)
	v_mfma_f32_16x16x32_bf16 v[74:77], v[158:161], v[30:33], v[74:77]
	v_mfma_f32_16x16x32_bf16 v[70:73], v[190:193], v[30:33], v[70:73]
	s_waitcnt lgkmcnt(2)
	v_mfma_f32_16x16x32_bf16 v[66:69], v[158:161], v[38:41], v[66:69]
	v_mfma_f32_16x16x32_bf16 v[62:65], v[190:193], v[38:41], v[62:65]
.LBB0_1350:
	s_waitcnt lgkmcnt(4)
	ds_read_b128 v[26:29], v243 offset:36864
	s_waitcnt lgkmcnt(4)
	ds_read_b128 v[30:33], v243 offset:40960
	s_waitcnt lgkmcnt(4)
	ds_read_b128 v[38:41], v243 offset:45056
.LBB0_1352:
	v_add_co_u32_e32 v122, vcc, 0x8000, v4
	s_nop 1
	v_addc_co_u32_e32 v123, vcc, 0, v5, vcc
	global_load_dwordx4 v[154:157], v[122:123], off offset:2048
	s_and_saveexec_b64 s[38:39], s[48:49]
	ds_write_b128 v235, v[6:9] offset:32768
	s_or_b64 exec, exec, s[38:39]
	s_waitcnt vmcnt(15) lgkmcnt(2)
	v_mfma_f32_16x16x32_bf16 v[58:61], v[158:161], v[198:201], v[58:61]
	s_waitcnt vmcnt(12)
	v_mfma_f32_16x16x32_bf16 v[54:57], v[190:193], v[198:201], v[54:57]
	v_mfma_f32_16x16x32_bf16 v[50:53], v[158:161], v[194:197], v[50:53]
	v_mfma_f32_16x16x32_bf16 v[46:49], v[190:193], v[194:197], v[46:49]
	s_waitcnt lgkmcnt(1)
	v_mfma_f32_16x16x32_bf16 v[42:45], v[158:161], v[202:205], v[42:45]
	v_mfma_f32_16x16x32_bf16 v[14:17], v[190:193], v[202:205], v[14:17]
.LBB0_1356:
	s_waitcnt lgkmcnt(2)
	ds_read_b128 v[198:201], v243 offset:49152
	ds_read_b128 v[194:197], v243 offset:53248
	s_waitcnt lgkmcnt(3)
	ds_read_b128 v[202:205], v243 offset:57344
.LBB0_1358:
	v_add_co_u32_e32 v4, vcc, 0x8000, v4
	s_nop 1
	v_addc_co_u32_e32 v5, vcc, 0, v5, vcc
	global_load_dwordx4 v[138:141], v[4:5], off offset:3072
	s_waitcnt vmcnt(14) lgkmcnt(2)
	v_mfma_f32_16x16x32_bf16 v[182:185], v[150:153], v[26:29], v[182:185]
	s_waitcnt vmcnt(12)
	v_mfma_f32_16x16x32_bf16 v[162:165], v[178:181], v[26:29], v[162:165]
	s_waitcnt lgkmcnt(1)
	v_mfma_f32_16x16x32_bf16 v[134:137], v[150:153], v[30:33], v[134:137]
	v_mfma_f32_16x16x32_bf16 v[118:121], v[178:181], v[30:33], v[118:121]
	s_waitcnt lgkmcnt(0)
	v_mfma_f32_16x16x32_bf16 v[102:105], v[150:153], v[38:41], v[102:105]
	v_mfma_f32_16x16x32_bf16 v[86:89], v[178:181], v[38:41], v[86:89]
.LBB0_1360:
	s_waitcnt lgkmcnt(1)
	ds_read_b128 v[30:33], v246 offset:28672
	ds_read_b128 v[26:29], v243 offset:61440
	s_waitcnt lgkmcnt(2)
	ds_read_b128 v[38:41], v246 offset:32768
.LBB0_1362:
	s_waitcnt vmcnt(14) lgkmcnt(2)
	v_mfma_f32_16x16x32_bf16 v[82:85], v[150:153], v[198:201], v[82:85]
	s_waitcnt vmcnt(12)
	v_mfma_f32_16x16x32_bf16 v[78:81], v[178:181], v[198:201], v[78:81]
	s_waitcnt lgkmcnt(1)
	v_mfma_f32_16x16x32_bf16 v[74:77], v[150:153], v[194:197], v[74:77]
	v_mfma_f32_16x16x32_bf16 v[70:73], v[178:181], v[194:197], v[70:73]
	s_waitcnt lgkmcnt(0)
	v_mfma_f32_16x16x32_bf16 v[66:69], v[150:153], v[202:205], v[66:69]
	v_mfma_f32_16x16x32_bf16 v[62:65], v[178:181], v[202:205], v[62:65]
.LBB0_1364:
	s_waitcnt vmcnt(14) lgkmcnt(1)
	v_mfma_f32_16x16x32_bf16 v[58:61], v[150:153], v[26:29], v[58:61]
	s_waitcnt vmcnt(12)
	v_mfma_f32_16x16x32_bf16 v[54:57], v[178:181], v[26:29], v[54:57]
	v_mfma_f32_16x16x32_bf16 v[50:53], v[150:153], v[30:33], v[50:53]
	v_mfma_f32_16x16x32_bf16 v[46:49], v[178:181], v[30:33], v[46:49]
	s_waitcnt lgkmcnt(0)
	v_mfma_f32_16x16x32_bf16 v[42:45], v[150:153], v[38:41], v[42:45]
	v_mfma_f32_16x16x32_bf16 v[14:17], v[178:181], v[38:41], v[14:17]
.LBB0_1366:
	s_add_i32 s75, s75, 1
	s_cmp_lg_u32 s75, 8
	s_cbranch_scc1 .LBB0_1263
	v_mov_b32_e32 v3, v236
	v_mov_b32_e32 v5, v237
	s_lshl_b32 s12, s74, 7
	s_add_i32 s12, s12, s65
	v_lshl_add_u32 v4, v3, 2, 0
	v_add_u32_e32 v4, 0x25500, v4
	v_lshl_add_u32 v130, v5, 2, s12
	ds_read2_b32 v[128:129], v4 offset1:16
	ds_read2_b32 v[126:127], v4 offset0:32 offset1:48
	ds_read2_b32 v[124:125], v4 offset0:64 offset1:80
	ds_read2_b32 v[122:123], v4 offset0:96 offset1:112
	ds_read_b32 v4, v4 offset:512
	v_lshrrev_b32_e32 v131, 7, v130
	v_lshrrev_b32_e32 v130, 3, v130
	v_mul_lo_u32 v144, v131, s80
	v_lshlrev_b32_e32 v145, 8, v3
	v_xor_b32_e32 v3, v130, v3
	s_waitcnt lgkmcnt(4)
	v_pk_mul_f32 v[130:131], v[182:183], v[128:129] op_sel_hi:[1,0]
	v_lshlrev_b32_e32 v3, 4, v3
	v_mul_f32_e32 v132, 0xbfb8aa3b, v130
	v_mul_f32_e32 v133, 0xbfb8aa3b, v131
	v_exp_f32_e32 v132, v132
	v_exp_f32_e32 v133, v133
	v_lshlrev_b32_e32 v5, 3, v5
	s_add_i32 s12, 0, 0x12000
	v_add_f32_e32 v132, 1.0, v132
	v_add_f32_e32 v133, 1.0, v133
	v_rcp_f32_e32 v132, v132
	v_rcp_f32_e32 v133, v133
	v_and_b32_e32 v3, 0xf0, v3
	v_and_b32_e32 v5, 8, v5
	s_waitcnt lgkmcnt(3)
	v_pk_mul_f32 v[102:103], v[102:103], v[126:127] op_sel_hi:[1,0]
	v_pk_mul_f32 v[130:131], v[130:131], v[132:133]
	v_pk_mul_f32 v[132:133], v[162:163], v[128:129] op_sel_hi:[1,0]
	v_pk_mul_f32 v[86:87], v[86:87], v[126:127] op_sel_hi:[1,0]
	v_pk_mul_f32 v[130:131], v[132:133], v[130:131]
	v_pk_mul_f32 v[132:133], v[184:185], v[128:129] op_sel_hi:[1,0]
	v_cvt_pk_bf16_f32 v130, v130, v131
	v_mul_f32_e32 v142, 0xbfb8aa3b, v132
	v_mul_f32_e32 v143, 0xbfb8aa3b, v133
	v_exp_f32_e32 v142, v142
	v_exp_f32_e32 v143, v143
	v_pk_mul_f32 v[88:89], v[88:89], v[126:127] op_sel_hi:[1,0]
	s_waitcnt lgkmcnt(2)
	v_pk_mul_f32 v[74:75], v[74:75], v[124:125] op_sel_hi:[1,0]
	v_add_f32_e32 v142, 1.0, v142
	v_add_f32_e32 v143, 1.0, v143
	v_rcp_f32_e32 v142, v142
	v_rcp_f32_e32 v143, v143
	v_pk_mul_f32 v[70:71], v[70:71], v[124:125] op_sel_hi:[1,0]
	v_pk_mul_f32 v[72:73], v[72:73], v[124:125] op_sel_hi:[1,0]
	s_waitcnt lgkmcnt(1)
	v_pk_mul_f32 v[58:59], v[58:59], v[122:123] op_sel_hi:[1,0]
	v_pk_mul_f32 v[132:133], v[132:133], v[142:143]
	v_pk_mul_f32 v[142:143], v[164:165], v[128:129] op_sel_hi:[1,0]
	v_add3_u32 v128, s12, v144, v145
	v_pk_mul_f32 v[132:133], v[142:143], v[132:133]
	v_add3_u32 v128, v128, v3, v5
	v_cvt_pk_bf16_f32 v131, v132, v133
	ds_write_b64 v128, v[130:131]
	v_mov_b32_e32 v128, v129
	v_pk_mul_f32 v[130:131], v[134:135], v[128:129] op_sel_hi:[1,0]
	v_pk_mul_f32 v[54:55], v[54:55], v[122:123] op_sel_hi:[1,0]
	v_mul_f32_e32 v129, 0xbfb8aa3b, v130
	v_exp_f32_e32 v129, v129
	v_pk_mul_f32 v[56:57], v[56:57], v[122:123] op_sel_hi:[1,0]
	s_add_i32 s74, s74, 1
	s_mov_b32 s75, 0
	v_add_f32_e32 v129, 1.0, v129
	v_rcp_f32_e32 v132, v129
	v_mul_f32_e32 v129, 0xbfb8aa3b, v131
	v_exp_f32_e32 v129, v129
	s_nop 0
	v_add_f32_e32 v129, 1.0, v129
	v_rcp_f32_e32 v133, v129
	v_pk_mul_f32 v[118:119], v[118:119], v[128:129] op_sel_hi:[1,0]
	v_pk_mul_f32 v[130:131], v[130:131], v[132:133]
	s_nop 0
	v_pk_mul_f32 v[118:119], v[118:119], v[130:131]
	v_pk_mul_f32 v[130:131], v[136:137], v[128:129] op_sel_hi:[1,0]
	v_cvt_pk_bf16_f32 v118, v118, v119
	v_mul_f32_e32 v129, 0xbfb8aa3b, v130
	v_exp_f32_e32 v129, v129
	s_nop 0
	v_add_f32_e32 v129, 1.0, v129
	v_rcp_f32_e32 v132, v129
	v_mul_f32_e32 v129, 0xbfb8aa3b, v131
	v_exp_f32_e32 v129, v129
	s_nop 0
	v_add_f32_e32 v129, 1.0, v129
	v_rcp_f32_e32 v133, v129
	v_pk_mul_f32 v[120:121], v[120:121], v[128:129] op_sel_hi:[1,0]
	v_pk_mul_f32 v[130:131], v[130:131], v[132:133]
	s_nop 0
	v_pk_mul_f32 v[120:121], v[120:121], v[130:131]
	s_nop 0
	v_cvt_pk_bf16_f32 v119, v120, v121
	v_add3_u32 v120, 0, v144, v145
	v_add3_u32 v3, v120, v3, v5
	v_add_u32_e32 v5, 0x13000, v3
	ds_write_b64 v5, v[118:119]
	v_mul_f32_e32 v5, 0xbfb8aa3b, v102
	v_exp_f32_e32 v5, v5
	s_nop 0
	v_add_f32_e32 v5, 1.0, v5
	v_rcp_f32_e32 v118, v5
	v_mul_f32_e32 v5, 0xbfb8aa3b, v103
	v_exp_f32_e32 v5, v5
	s_nop 0
	v_add_f32_e32 v5, 1.0, v5
	v_rcp_f32_e32 v119, v5
	s_nop 0
	v_pk_mul_f32 v[102:103], v[102:103], v[118:119]
	s_nop 0
	v_pk_mul_f32 v[86:87], v[86:87], v[102:103]
	v_pk_mul_f32 v[102:103], v[104:105], v[126:127] op_sel_hi:[1,0]
	v_cvt_pk_bf16_f32 v86, v86, v87
	v_mul_f32_e32 v5, 0xbfb8aa3b, v102
	v_exp_f32_e32 v5, v5
	s_nop 0
	v_add_f32_e32 v5, 1.0, v5
	v_rcp_f32_e32 v104, v5
	v_mul_f32_e32 v5, 0xbfb8aa3b, v103
	v_exp_f32_e32 v5, v5
	s_nop 0
	v_add_f32_e32 v5, 1.0, v5
	v_rcp_f32_e32 v105, v5
	v_add_u32_e32 v5, 0x14000, v3
	v_pk_mul_f32 v[102:103], v[102:103], v[104:105]
	s_nop 0
	v_pk_mul_f32 v[88:89], v[88:89], v[102:103]
	s_nop 0
	v_cvt_pk_bf16_f32 v87, v88, v89
	ds_write_b64 v5, v[86:87]
	v_mov_b32_e32 v86, v127
	v_pk_mul_f32 v[82:83], v[82:83], v[86:87] op_sel_hi:[1,0]
	v_pk_mul_f32 v[78:79], v[78:79], v[86:87] op_sel_hi:[1,0]
	v_mul_f32_e32 v5, 0xbfb8aa3b, v82
	v_exp_f32_e32 v5, v5
	v_pk_mul_f32 v[80:81], v[80:81], v[86:87] op_sel_hi:[1,0]
	v_add_f32_e32 v5, 1.0, v5
	v_rcp_f32_e32 v88, v5
	v_mul_f32_e32 v5, 0xbfb8aa3b, v83
	v_exp_f32_e32 v5, v5
	s_nop 0
	v_add_f32_e32 v5, 1.0, v5
	v_rcp_f32_e32 v89, v5
	s_nop 0
	v_pk_mul_f32 v[82:83], v[82:83], v[88:89]
	s_nop 0
	v_pk_mul_f32 v[78:79], v[78:79], v[82:83]
	v_pk_mul_f32 v[82:83], v[84:85], v[86:87] op_sel_hi:[1,0]
	v_cvt_pk_bf16_f32 v78, v78, v79
	v_mul_f32_e32 v5, 0xbfb8aa3b, v82
	v_exp_f32_e32 v5, v5
	s_nop 0
	v_add_f32_e32 v5, 1.0, v5
	v_rcp_f32_e32 v84, v5
	v_mul_f32_e32 v5, 0xbfb8aa3b, v83
	v_exp_f32_e32 v5, v5
	s_nop 0
	v_add_f32_e32 v5, 1.0, v5
	v_rcp_f32_e32 v85, v5
	v_add_u32_e32 v5, 0x15000, v3
	v_pk_mul_f32 v[82:83], v[82:83], v[84:85]
	s_nop 0
	v_pk_mul_f32 v[80:81], v[80:81], v[82:83]
	s_nop 0
	v_cvt_pk_bf16_f32 v79, v80, v81
	ds_write_b64 v5, v[78:79]
	v_mul_f32_e32 v5, 0xbfb8aa3b, v74
	v_exp_f32_e32 v5, v5
	s_nop 0
	v_add_f32_e32 v5, 1.0, v5
	v_rcp_f32_e32 v78, v5
	v_mul_f32_e32 v5, 0xbfb8aa3b, v75
	v_exp_f32_e32 v5, v5
	s_nop 0
	v_add_f32_e32 v5, 1.0, v5
	v_rcp_f32_e32 v79, v5
	s_nop 0
	v_pk_mul_f32 v[74:75], v[74:75], v[78:79]
	s_nop 0
	v_pk_mul_f32 v[70:71], v[70:71], v[74:75]
	v_pk_mul_f32 v[74:75], v[76:77], v[124:125] op_sel_hi:[1,0]
	v_cvt_pk_bf16_f32 v70, v70, v71
	v_mul_f32_e32 v5, 0xbfb8aa3b, v74
	v_exp_f32_e32 v5, v5
	s_nop 0
	v_add_f32_e32 v5, 1.0, v5
	v_rcp_f32_e32 v76, v5
	v_mul_f32_e32 v5, 0xbfb8aa3b, v75
	v_exp_f32_e32 v5, v5
	s_nop 0
	v_add_f32_e32 v5, 1.0, v5
	v_rcp_f32_e32 v77, v5
	v_add_u32_e32 v5, 0x16000, v3
	v_pk_mul_f32 v[74:75], v[74:75], v[76:77]
	s_nop 0
	v_pk_mul_f32 v[72:73], v[72:73], v[74:75]
	s_nop 0
	v_cvt_pk_bf16_f32 v71, v72, v73
	ds_write_b64 v5, v[70:71]
	v_mov_b32_e32 v70, v125
	v_pk_mul_f32 v[66:67], v[66:67], v[70:71] op_sel_hi:[1,0]
	v_pk_mul_f32 v[62:63], v[62:63], v[70:71] op_sel_hi:[1,0]
	v_mul_f32_e32 v5, 0xbfb8aa3b, v66
	v_exp_f32_e32 v5, v5
	v_pk_mul_f32 v[64:65], v[64:65], v[70:71] op_sel_hi:[1,0]
	v_add_f32_e32 v5, 1.0, v5
	v_rcp_f32_e32 v72, v5
	v_mul_f32_e32 v5, 0xbfb8aa3b, v67
	v_exp_f32_e32 v5, v5
	s_nop 0
	v_add_f32_e32 v5, 1.0, v5
	v_rcp_f32_e32 v73, v5
	s_nop 0
	v_pk_mul_f32 v[66:67], v[66:67], v[72:73]
	s_nop 0
	v_pk_mul_f32 v[62:63], v[62:63], v[66:67]
	v_pk_mul_f32 v[66:67], v[68:69], v[70:71] op_sel_hi:[1,0]
	v_cvt_pk_bf16_f32 v62, v62, v63
	v_mul_f32_e32 v5, 0xbfb8aa3b, v66
	v_exp_f32_e32 v5, v5
	s_nop 0
	v_add_f32_e32 v5, 1.0, v5
	v_rcp_f32_e32 v68, v5
	v_mul_f32_e32 v5, 0xbfb8aa3b, v67
	v_exp_f32_e32 v5, v5
	s_nop 0
	v_add_f32_e32 v5, 1.0, v5
	v_rcp_f32_e32 v69, v5
	v_add_u32_e32 v5, 0x17000, v3
	v_pk_mul_f32 v[66:67], v[66:67], v[68:69]
	s_nop 0
	v_pk_mul_f32 v[64:65], v[64:65], v[66:67]
	s_nop 0
	v_cvt_pk_bf16_f32 v63, v64, v65
	ds_write_b64 v5, v[62:63]
	v_mul_f32_e32 v5, 0xbfb8aa3b, v58
	v_exp_f32_e32 v5, v5
	s_nop 0
	v_add_f32_e32 v5, 1.0, v5
	v_rcp_f32_e32 v62, v5
	v_mul_f32_e32 v5, 0xbfb8aa3b, v59
	v_exp_f32_e32 v5, v5
	s_nop 0
	v_add_f32_e32 v5, 1.0, v5
	v_rcp_f32_e32 v63, v5
	s_nop 0
	v_pk_mul_f32 v[58:59], v[58:59], v[62:63]
	s_nop 0
	v_pk_mul_f32 v[54:55], v[54:55], v[58:59]
	v_pk_mul_f32 v[58:59], v[60:61], v[122:123] op_sel_hi:[1,0]
	v_cvt_pk_bf16_f32 v54, v54, v55
	v_mul_f32_e32 v5, 0xbfb8aa3b, v58
	v_exp_f32_e32 v5, v5
	s_nop 0
	v_add_f32_e32 v5, 1.0, v5
	v_rcp_f32_e32 v60, v5
	v_mul_f32_e32 v5, 0xbfb8aa3b, v59
	v_exp_f32_e32 v5, v5
	s_nop 0
	v_add_f32_e32 v5, 1.0, v5
	v_rcp_f32_e32 v61, v5
	v_add_u32_e32 v5, 0x18000, v3
	v_pk_mul_f32 v[58:59], v[58:59], v[60:61]
	s_nop 0
	v_pk_mul_f32 v[56:57], v[56:57], v[58:59]
	s_nop 0
	v_cvt_pk_bf16_f32 v55, v56, v57
	ds_write_b64 v5, v[54:55]
	v_mov_b32_e32 v54, v123
	v_pk_mul_f32 v[50:51], v[50:51], v[54:55] op_sel_hi:[1,0]
	v_pk_mul_f32 v[46:47], v[46:47], v[54:55] op_sel_hi:[1,0]
	v_mul_f32_e32 v5, 0xbfb8aa3b, v50
	v_exp_f32_e32 v5, v5
	v_pk_mul_f32 v[48:49], v[48:49], v[54:55] op_sel_hi:[1,0]
	v_add_f32_e32 v5, 1.0, v5
	v_rcp_f32_e32 v56, v5
	v_mul_f32_e32 v5, 0xbfb8aa3b, v51
	v_exp_f32_e32 v5, v5
	s_nop 0
	v_add_f32_e32 v5, 1.0, v5
	v_rcp_f32_e32 v57, v5
	s_nop 0
	v_pk_mul_f32 v[50:51], v[50:51], v[56:57]
	s_nop 0
	v_pk_mul_f32 v[46:47], v[46:47], v[50:51]
	v_pk_mul_f32 v[50:51], v[52:53], v[54:55] op_sel_hi:[1,0]
	v_cvt_pk_bf16_f32 v46, v46, v47
	v_mul_f32_e32 v5, 0xbfb8aa3b, v50
	v_exp_f32_e32 v5, v5
	s_nop 0
	v_add_f32_e32 v5, 1.0, v5
	v_rcp_f32_e32 v52, v5
	v_mul_f32_e32 v5, 0xbfb8aa3b, v51
	v_exp_f32_e32 v5, v5
	s_nop 0
	v_add_f32_e32 v5, 1.0, v5
	v_rcp_f32_e32 v53, v5
	v_add_u32_e32 v5, 0x19000, v3
	s_waitcnt lgkmcnt(7)
	v_pk_mul_f32 v[42:43], v[42:43], v[4:5] op_sel_hi:[1,0]
	v_add_u32_e32 v3, 0x1a000, v3
	v_pk_mul_f32 v[50:51], v[50:51], v[52:53]
	s_nop 0
	v_pk_mul_f32 v[48:49], v[48:49], v[50:51]
	s_nop 0
	v_cvt_pk_bf16_f32 v47, v48, v49
	ds_write_b64 v5, v[46:47]
	v_mul_f32_e32 v5, 0xbfb8aa3b, v42
	v_exp_f32_e32 v5, v5
	s_nop 0
	v_add_f32_e32 v5, 1.0, v5
	v_rcp_f32_e32 v46, v5
	v_mul_f32_e32 v5, 0xbfb8aa3b, v43
	v_exp_f32_e32 v5, v5
	s_nop 0
	v_add_f32_e32 v5, 1.0, v5
	v_rcp_f32_e32 v47, v5
	v_pk_mul_f32 v[14:15], v[14:15], v[4:5] op_sel_hi:[1,0]
	v_pk_mul_f32 v[42:43], v[42:43], v[46:47]
	s_nop 0
	v_pk_mul_f32 v[14:15], v[14:15], v[42:43]
	v_pk_mul_f32 v[42:43], v[44:45], v[4:5] op_sel_hi:[1,0]
	v_cvt_pk_bf16_f32 v14, v14, v15
	v_mul_f32_e32 v5, 0xbfb8aa3b, v42
	v_exp_f32_e32 v5, v5
	s_nop 0
	v_add_f32_e32 v5, 1.0, v5
	v_rcp_f32_e32 v44, v5
	v_mul_f32_e32 v5, 0xbfb8aa3b, v43
	v_exp_f32_e32 v5, v5
	s_nop 0
	v_add_f32_e32 v5, 1.0, v5
	v_rcp_f32_e32 v45, v5
	v_pk_mul_f32 v[4:5], v[16:17], v[4:5] op_sel_hi:[1,0]
	v_pk_mul_f32 v[42:43], v[42:43], v[44:45]
	s_nop 0
	v_pk_mul_f32 v[4:5], v[4:5], v[42:43]
	s_nop 0
	v_cvt_pk_bf16_f32 v15, v4, v5
	v_mov_b32_e32 v4, v2
	v_mov_b32_e32 v5, v2
	ds_write_b64 v3, v[14:15]
	v_mov_b32_e32 v3, v2
	v_mov_b64_e32 v[16:17], v[4:5]
	v_mov_b64_e32 v[44:45], v[4:5]
	v_mov_b64_e32 v[48:49], v[4:5]
	v_mov_b64_e32 v[52:53], v[4:5]
	v_mov_b64_e32 v[56:57], v[4:5]
	v_mov_b64_e32 v[60:61], v[4:5]
	v_mov_b64_e32 v[64:65], v[4:5]
	v_mov_b64_e32 v[68:69], v[4:5]
	v_mov_b64_e32 v[72:73], v[4:5]
	v_mov_b64_e32 v[76:77], v[4:5]
	v_mov_b64_e32 v[80:81], v[4:5]
	v_mov_b64_e32 v[84:85], v[4:5]
	v_mov_b64_e32 v[88:89], v[4:5]
	v_mov_b64_e32 v[104:105], v[4:5]
	v_mov_b64_e32 v[120:121], v[4:5]
	v_mov_b64_e32 v[136:137], v[4:5]
	v_mov_b64_e32 v[164:165], v[4:5]
	v_mov_b64_e32 v[184:185], v[4:5]
	v_mov_b64_e32 v[14:15], v[2:3]
	v_mov_b64_e32 v[42:43], v[2:3]
	v_mov_b64_e32 v[46:47], v[2:3]
	v_mov_b64_e32 v[50:51], v[2:3]
	v_mov_b64_e32 v[54:55], v[2:3]
	v_mov_b64_e32 v[58:59], v[2:3]
	v_mov_b64_e32 v[62:63], v[2:3]
	v_mov_b64_e32 v[66:67], v[2:3]
	v_mov_b64_e32 v[70:71], v[2:3]
	v_mov_b64_e32 v[74:75], v[2:3]
	v_mov_b64_e32 v[78:79], v[2:3]
	v_mov_b64_e32 v[82:83], v[2:3]
	v_mov_b64_e32 v[86:87], v[2:3]
	v_mov_b64_e32 v[102:103], v[2:3]
	v_mov_b64_e32 v[118:119], v[2:3]
	v_mov_b64_e32 v[134:135], v[2:3]
	v_mov_b64_e32 v[162:163], v[2:3]
	v_mov_b64_e32 v[182:183], v[2:3]
	s_branch .LBB0_1263

.LBB0_1370:
	v_add_u32_e32 v30, v170, v171
	ds_read_b128 v[158:161], v30
	s_waitcnt vmcnt(9)
	ds_read_b128 v[154:157], v30 offset:4096
	ds_read_b128 v[162:165], v30 offset:8192
	ds_read_b128 v[6:9], v30 offset:12288
	ds_read_b128 v[10:13], v30 offset:16384
	ds_read_b128 v[22:25], v30 offset:20480
.LBB0_1372:
	v_mov_b32_e32 v4, v2
	v_mov_b32_e32 v5, v2
	v_mov_b32_e32 v3, v2
	v_mov_b64_e32 v[72:73], v[4:5]
	v_mov_b64_e32 v[76:77], v[4:5]
	v_mov_b64_e32 v[88:89], v[4:5]
	v_mov_b64_e32 v[92:93], v[4:5]
	v_mov_b64_e32 v[100:101], v[4:5]
	v_mov_b64_e32 v[104:105], v[4:5]
	v_mov_b64_e32 v[70:71], v[2:3]
	v_mov_b64_e32 v[74:75], v[2:3]
	v_mov_b64_e32 v[86:87], v[2:3]
	v_mov_b64_e32 v[90:91], v[2:3]
	v_mov_b64_e32 v[98:99], v[2:3]
	v_mov_b64_e32 v[102:103], v[2:3]
	s_waitcnt vmcnt(7) lgkmcnt(2)
	v_mfma_f32_16x16x32_bf16 v[102:105], v[126:129], v[158:161], 0
	s_waitcnt vmcnt(3)
	v_mfma_f32_16x16x32_bf16 v[98:101], v[130:133], v[158:161], 0
	s_waitcnt lgkmcnt(1)
	v_mfma_f32_16x16x32_bf16 v[90:93], v[126:129], v[154:157], 0
	v_mfma_f32_16x16x32_bf16 v[86:89], v[130:133], v[154:157], 0
	s_waitcnt lgkmcnt(0)
	v_mfma_f32_16x16x32_bf16 v[74:77], v[126:129], v[162:165], 0
	v_mfma_f32_16x16x32_bf16 v[70:73], v[130:133], v[162:165], 0
.LBB0_1374:
	s_waitcnt lgkmcnt(1)
	ds_read_b128 v[154:157], v30 offset:28672
	ds_read_b128 v[158:161], v30 offset:24576
	s_waitcnt lgkmcnt(2)
	ds_read_b128 v[162:165], v30 offset:32768
.LBB0_1376:
	v_mov_b32_e32 v4, v2
	v_mov_b32_e32 v5, v2
	v_mov_b32_e32 v3, v2
	v_mov_b64_e32 v[48:49], v[4:5]
	v_mov_b64_e32 v[52:53], v[4:5]
	v_mov_b64_e32 v[64:65], v[4:5]
	v_mov_b64_e32 v[68:69], v[4:5]
	v_mov_b64_e32 v[80:81], v[4:5]
	v_mov_b64_e32 v[84:85], v[4:5]
	v_mov_b64_e32 v[46:47], v[2:3]
	v_mov_b64_e32 v[50:51], v[2:3]
	v_mov_b64_e32 v[62:63], v[2:3]
	v_mov_b64_e32 v[66:67], v[2:3]
	v_mov_b64_e32 v[78:79], v[2:3]
	v_mov_b64_e32 v[82:83], v[2:3]
	s_waitcnt vmcnt(7) lgkmcnt(2)
	v_mfma_f32_16x16x32_bf16 v[82:85], v[126:129], v[6:9], 0
	s_waitcnt vmcnt(3)
	v_mfma_f32_16x16x32_bf16 v[78:81], v[130:133], v[6:9], 0
	s_waitcnt lgkmcnt(1)
	v_mfma_f32_16x16x32_bf16 v[66:69], v[126:129], v[10:13], 0
	v_mfma_f32_16x16x32_bf16 v[62:65], v[130:133], v[10:13], 0
	s_waitcnt lgkmcnt(0)
	v_mfma_f32_16x16x32_bf16 v[50:53], v[126:129], v[22:25], 0
	v_mfma_f32_16x16x32_bf16 v[46:49], v[130:133], v[22:25], 0
.LBB0_1378:
	v_add_u32_e32 v134, v170, v173
	s_waitcnt lgkmcnt(2)
	ds_read_b128 v[6:9], v134
	s_waitcnt lgkmcnt(2)
	ds_read_b128 v[10:13], v134 offset:4096
	s_waitcnt lgkmcnt(2)
	ds_read_b128 v[22:25], v134 offset:8192
.LBB0_1380:
	v_mov_b32_e32 v4, v2
	v_mov_b32_e32 v5, v2
	v_mov_b32_e32 v3, v2
	v_mov_b64_e32 v[32:33], v[4:5]
	v_mov_b64_e32 v[36:37], v[4:5]
	v_mov_b64_e32 v[40:41], v[4:5]
	v_mov_b64_e32 v[44:45], v[4:5]
	v_mov_b64_e32 v[56:57], v[4:5]
	v_mov_b64_e32 v[60:61], v[4:5]
	v_mov_b64_e32 v[30:31], v[2:3]
	v_mov_b64_e32 v[34:35], v[2:3]
	v_mov_b64_e32 v[38:39], v[2:3]
	v_mov_b64_e32 v[42:43], v[2:3]
	v_mov_b64_e32 v[54:55], v[2:3]
	v_mov_b64_e32 v[58:59], v[2:3]
	s_waitcnt vmcnt(7) lgkmcnt(1)
	v_mfma_f32_16x16x32_bf16 v[58:61], v[126:129], v[158:161], 0
	s_waitcnt vmcnt(3)
	v_mfma_f32_16x16x32_bf16 v[54:57], v[130:133], v[158:161], 0
	v_mfma_f32_16x16x32_bf16 v[42:45], v[126:129], v[154:157], 0
	v_mfma_f32_16x16x32_bf16 v[38:41], v[130:133], v[154:157], 0
	s_waitcnt lgkmcnt(0)
	v_mfma_f32_16x16x32_bf16 v[34:37], v[126:129], v[162:165], 0
	v_mfma_f32_16x16x32_bf16 v[30:33], v[130:133], v[162:165], 0
.LBB0_1382:
	s_waitcnt lgkmcnt(1)
	ds_read_b128 v[158:161], v134 offset:12288
	ds_read_b128 v[154:157], v134 offset:16384
	s_waitcnt lgkmcnt(2)
	ds_read_b128 v[162:165], v134 offset:20480
.LBB0_1384:
	s_ashr_i32 s65, s64, 31
	s_lshl_b32 s20, s73, 2
	s_lshl_b64 s[38:39], s[64:65], 17
	s_lshl_b64 s[74:75], s[20:21], 10
	v_lshl_add_u64 v[4:5], v[166:167], 0, s[38:39]
	v_lshl_add_u64 v[4:5], v[4:5], 0, s[74:75]
	s_waitcnt vmcnt(3)
	v_add_co_u32_e32 v130, vcc, 0x2000, v4
	s_nop 1
	v_addc_co_u32_e32 v131, vcc, 0, v5, vcc
	global_load_dwordx4 v[126:129], v[4:5], off
	s_nop 0
	global_load_dwordx4 v[130:133], v[130:131], off
	s_waitcnt lgkmcnt(2)
	v_mfma_f32_16x16x32_bf16 v[102:105], v[114:117], v[6:9], v[102:105]
	s_waitcnt vmcnt(4)
	v_mfma_f32_16x16x32_bf16 v[98:101], v[122:125], v[6:9], v[98:101]
	s_waitcnt lgkmcnt(1)
	v_mfma_f32_16x16x32_bf16 v[90:93], v[114:117], v[10:13], v[90:93]
	v_mfma_f32_16x16x32_bf16 v[86:89], v[122:125], v[10:13], v[86:89]
	s_waitcnt lgkmcnt(0)
	v_mfma_f32_16x16x32_bf16 v[74:77], v[114:117], v[22:25], v[74:77]
	v_mfma_f32_16x16x32_bf16 v[70:73], v[122:125], v[22:25], v[70:73]
.LBB0_1386:
	s_waitcnt lgkmcnt(1)
	ds_read_b128 v[10:13], v134 offset:28672
	ds_read_b128 v[6:9], v134 offset:24576
	s_waitcnt lgkmcnt(2)
	ds_read_b128 v[22:25], v134 offset:32768
.LBB0_1388:
	global_load_dwordx4 v[146:149], v[4:5], off offset:1024
	s_waitcnt lgkmcnt(1)
	v_mfma_f32_16x16x32_bf16 v[82:85], v[114:117], v[158:161], v[82:85]
	s_waitcnt vmcnt(5)
	v_mfma_f32_16x16x32_bf16 v[78:81], v[122:125], v[158:161], v[78:81]
	v_mfma_f32_16x16x32_bf16 v[66:69], v[114:117], v[154:157], v[66:69]
	v_mfma_f32_16x16x32_bf16 v[62:65], v[122:125], v[154:157], v[62:65]
	s_waitcnt lgkmcnt(0)
	v_mfma_f32_16x16x32_bf16 v[50:53], v[114:117], v[162:165], v[50:53]
	v_mfma_f32_16x16x32_bf16 v[46:49], v[122:125], v[162:165], v[46:49]
.LBB0_1390:
	v_add_u32_e32 v3, v170, v174
	s_waitcnt lgkmcnt(1)
	ds_read_b128 v[158:161], v3
	ds_read_b128 v[154:157], v3 offset:4096
	s_waitcnt lgkmcnt(2)
	ds_read_b128 v[162:165], v3 offset:8192
.LBB0_1392:
	global_load_dwordx4 v[138:141], v[4:5], off offset:2048
	s_waitcnt lgkmcnt(1)
	v_mfma_f32_16x16x32_bf16 v[58:61], v[114:117], v[6:9], v[58:61]
	s_waitcnt vmcnt(6)
	v_mfma_f32_16x16x32_bf16 v[54:57], v[122:125], v[6:9], v[54:57]
	v_mfma_f32_16x16x32_bf16 v[42:45], v[114:117], v[10:13], v[42:45]
	v_mfma_f32_16x16x32_bf16 v[38:41], v[122:125], v[10:13], v[38:41]
	s_waitcnt lgkmcnt(0)
	v_mfma_f32_16x16x32_bf16 v[34:37], v[114:117], v[22:25], v[34:37]
	v_mfma_f32_16x16x32_bf16 v[30:33], v[122:125], v[22:25], v[30:33]
.LBB0_1394:
	s_waitcnt lgkmcnt(1)
	ds_read_b128 v[6:9], v3 offset:12288
	ds_read_b128 v[10:13], v3 offset:16384
	s_waitcnt lgkmcnt(2)
	ds_read_b128 v[22:25], v3 offset:20480
.LBB0_1396:
	v_add_co_u32_e32 v114, vcc, 0x2000, v4
	s_nop 1
	v_addc_co_u32_e32 v115, vcc, 0, v5, vcc
	global_load_dwordx4 v[122:125], v[114:115], off offset:1024
	s_waitcnt lgkmcnt(1)
	v_mfma_f32_16x16x32_bf16 v[102:105], v[106:109], v[158:161], v[102:105]
	s_waitcnt vmcnt(6)
	v_mfma_f32_16x16x32_bf16 v[98:101], v[118:121], v[158:161], v[98:101]
	v_mfma_f32_16x16x32_bf16 v[90:93], v[106:109], v[154:157], v[90:93]
	v_mfma_f32_16x16x32_bf16 v[86:89], v[118:121], v[154:157], v[86:89]
	s_waitcnt lgkmcnt(0)
	v_mfma_f32_16x16x32_bf16 v[74:77], v[106:109], v[162:165], v[74:77]
	v_mfma_f32_16x16x32_bf16 v[70:73], v[118:121], v[162:165], v[70:73]
.LBB0_1398:
	s_waitcnt lgkmcnt(1)
	ds_read_b128 v[154:157], v3 offset:28672
	ds_read_b128 v[158:161], v3 offset:24576
	s_waitcnt lgkmcnt(2)
	ds_read_b128 v[162:165], v3 offset:32768
.LBB0_1400:
	global_load_dwordx4 v[134:137], v[4:5], off offset:3072
	s_waitcnt lgkmcnt(1)
	v_mfma_f32_16x16x32_bf16 v[82:85], v[106:109], v[6:9], v[82:85]
	s_waitcnt vmcnt(7)
	v_mfma_f32_16x16x32_bf16 v[78:81], v[118:121], v[6:9], v[78:81]
	v_mfma_f32_16x16x32_bf16 v[66:69], v[106:109], v[10:13], v[66:69]
	v_mfma_f32_16x16x32_bf16 v[62:65], v[118:121], v[10:13], v[62:65]
	s_waitcnt lgkmcnt(0)
	v_mfma_f32_16x16x32_bf16 v[50:53], v[106:109], v[22:25], v[50:53]
	v_mfma_f32_16x16x32_bf16 v[46:49], v[118:121], v[22:25], v[46:49]
.LBB0_1402:
	v_add_u32_e32 v3, v170, v175
	s_waitcnt lgkmcnt(1)
	ds_read_b128 v[6:9], v3
	ds_read_b128 v[10:13], v3 offset:4096
	s_waitcnt lgkmcnt(2)
	ds_read_b128 v[22:25], v3 offset:8192
.LBB0_1404:
	v_add_co_u32_e32 v114, vcc, 0x2000, v4
	s_nop 1
	v_addc_co_u32_e32 v115, vcc, 0, v5, vcc
	global_load_dwordx4 v[150:153], v[114:115], off offset:2048
	s_waitcnt lgkmcnt(1)
	v_mfma_f32_16x16x32_bf16 v[58:61], v[106:109], v[158:161], v[58:61]
	s_waitcnt vmcnt(8)
	v_mfma_f32_16x16x32_bf16 v[54:57], v[118:121], v[158:161], v[54:57]
	v_mfma_f32_16x16x32_bf16 v[42:45], v[106:109], v[154:157], v[42:45]
	v_mfma_f32_16x16x32_bf16 v[38:41], v[118:121], v[154:157], v[38:41]
	s_waitcnt lgkmcnt(0)
	v_mfma_f32_16x16x32_bf16 v[34:37], v[106:109], v[162:165], v[34:37]
	v_mfma_f32_16x16x32_bf16 v[30:33], v[118:121], v[162:165], v[30:33]
.LBB0_1406:
	s_waitcnt lgkmcnt(1)
	ds_read_b128 v[158:161], v3 offset:12288
	ds_read_b128 v[154:157], v3 offset:16384
	s_waitcnt lgkmcnt(2)
	ds_read_b128 v[162:165], v3 offset:20480
.LBB0_1408:
	v_add_co_u32_e32 v4, vcc, 0x2000, v4
	s_nop 1
	v_addc_co_u32_e32 v5, vcc, 0, v5, vcc
	global_load_dwordx4 v[142:145], v[4:5], off offset:3072
	s_waitcnt vmcnt(10) lgkmcnt(1)
	v_mfma_f32_16x16x32_bf16 v[102:105], v[94:97], v[6:9], v[102:105]
	s_waitcnt vmcnt(8)
	v_mfma_f32_16x16x32_bf16 v[98:101], v[110:113], v[6:9], v[98:101]
	v_mfma_f32_16x16x32_bf16 v[90:93], v[94:97], v[10:13], v[90:93]
	v_mfma_f32_16x16x32_bf16 v[86:89], v[110:113], v[10:13], v[86:89]
	s_waitcnt lgkmcnt(0)
	v_mfma_f32_16x16x32_bf16 v[74:77], v[94:97], v[22:25], v[74:77]
	v_mfma_f32_16x16x32_bf16 v[70:73], v[110:113], v[22:25], v[70:73]
.LBB0_1410:
	s_waitcnt lgkmcnt(1)
	ds_read_b128 v[10:13], v3 offset:28672
	ds_read_b128 v[6:9], v3 offset:24576
	s_waitcnt lgkmcnt(2)
	ds_read_b128 v[22:25], v3 offset:32768
.LBB0_1412:
	s_waitcnt vmcnt(10) lgkmcnt(1)
	v_mfma_f32_16x16x32_bf16 v[82:85], v[94:97], v[158:161], v[82:85]
	s_waitcnt vmcnt(8)
	v_mfma_f32_16x16x32_bf16 v[78:81], v[110:113], v[158:161], v[78:81]
	v_mfma_f32_16x16x32_bf16 v[66:69], v[94:97], v[154:157], v[66:69]
	v_mfma_f32_16x16x32_bf16 v[62:65], v[110:113], v[154:157], v[62:65]
	s_waitcnt lgkmcnt(0)
	v_mfma_f32_16x16x32_bf16 v[50:53], v[94:97], v[162:165], v[50:53]
	v_mfma_f32_16x16x32_bf16 v[46:49], v[110:113], v[162:165], v[46:49]
.LBB0_1414:
	s_waitcnt vmcnt(10) lgkmcnt(1)
	v_mfma_f32_16x16x32_bf16 v[58:61], v[94:97], v[6:9], v[58:61]
	s_waitcnt vmcnt(8)
	v_mfma_f32_16x16x32_bf16 v[54:57], v[110:113], v[6:9], v[54:57]
	v_mfma_f32_16x16x32_bf16 v[42:45], v[94:97], v[10:13], v[42:45]
	v_mfma_f32_16x16x32_bf16 v[38:41], v[110:113], v[10:13], v[38:41]
	s_waitcnt lgkmcnt(0)
	v_mfma_f32_16x16x32_bf16 v[34:37], v[94:97], v[22:25], v[34:37]
	v_mfma_f32_16x16x32_bf16 v[30:33], v[110:113], v[22:25], v[30:33]
.LBB0_1416:
	v_add_u32_e32 v3, v172, v171
	s_waitcnt lgkmcnt(0)
	s_barrier
	ds_read_b128 v[158:161], v3
	ds_read_b128 v[154:157], v3 offset:4096
	ds_read_b128 v[162:165], v3 offset:8192
	ds_read_b128 v[14:17], v3 offset:12288
	ds_read_b128 v[18:21], v3 offset:16384
	ds_read_b128 v[26:29], v3 offset:20480
.LBB0_1418:
	s_waitcnt vmcnt(7) lgkmcnt(2)
	v_mfma_f32_16x16x32_bf16 v[102:105], v[126:129], v[158:161], v[102:105]
	s_waitcnt vmcnt(6)
	v_mfma_f32_16x16x32_bf16 v[98:101], v[130:133], v[158:161], v[98:101]
	s_waitcnt lgkmcnt(1)
	v_mfma_f32_16x16x32_bf16 v[90:93], v[126:129], v[154:157], v[90:93]
	v_mfma_f32_16x16x32_bf16 v[86:89], v[130:133], v[154:157], v[86:89]
	s_waitcnt lgkmcnt(0)
	v_mfma_f32_16x16x32_bf16 v[74:77], v[126:129], v[162:165], v[74:77]
	v_mfma_f32_16x16x32_bf16 v[70:73], v[130:133], v[162:165], v[70:73]

.LBB0_1422:
	s_waitcnt vmcnt(7) lgkmcnt(2)
	v_mfma_f32_16x16x32_bf16 v[82:85], v[126:129], v[14:17], v[82:85]
	s_waitcnt vmcnt(6)
	v_mfma_f32_16x16x32_bf16 v[78:81], v[130:133], v[14:17], v[78:81]
	s_waitcnt lgkmcnt(1)
	v_mfma_f32_16x16x32_bf16 v[66:69], v[126:129], v[18:21], v[66:69]
	v_mfma_f32_16x16x32_bf16 v[62:65], v[130:133], v[18:21], v[62:65]
	s_waitcnt lgkmcnt(0)
	v_mfma_f32_16x16x32_bf16 v[50:53], v[126:129], v[26:29], v[50:53]
	v_mfma_f32_16x16x32_bf16 v[46:49], v[130:133], v[26:29], v[46:49]
.LBB0_1424:
	v_add_u32_e32 v3, v172, v173
	s_waitcnt lgkmcnt(2)
	ds_read_b128 v[14:17], v3
	s_waitcnt lgkmcnt(2)
	ds_read_b128 v[18:21], v3 offset:4096
	s_waitcnt lgkmcnt(2)
	ds_read_b128 v[26:29], v3 offset:8192
.LBB0_1426:
	s_waitcnt vmcnt(7) lgkmcnt(1)
	v_mfma_f32_16x16x32_bf16 v[58:61], v[126:129], v[158:161], v[58:61]
	s_waitcnt vmcnt(6)
	v_mfma_f32_16x16x32_bf16 v[54:57], v[130:133], v[158:161], v[54:57]
	v_mfma_f32_16x16x32_bf16 v[42:45], v[126:129], v[154:157], v[42:45]
	v_mfma_f32_16x16x32_bf16 v[38:41], v[130:133], v[154:157], v[38:41]
	s_waitcnt lgkmcnt(0)
	v_mfma_f32_16x16x32_bf16 v[34:37], v[126:129], v[162:165], v[34:37]
	v_mfma_f32_16x16x32_bf16 v[30:33], v[130:133], v[162:165], v[30:33]

.LBB0_1430:
	s_cmp_lt_i32 s64, 3
	s_cselect_b64 s[38:39], -1, 0
	s_and_b64 s[74:75], s[38:39], exec
	s_cselect_b32 s12, 0, s73
	s_cmp_gt_i32 s73, 0
	s_cselect_b64 s[74:75], -1, 0
	s_and_b64 s[76:77], s[74:75], exec
	s_cselect_b32 s73, s12, 1
	s_and_b64 s[38:39], s[74:75], s[38:39]
	s_cmp_lg_u64 s[38:39], 0
	s_addc_u32 s64, s64, 0
	s_ashr_i32 s65, s64, 31
	s_lshl_b32 s20, s73, 2
	s_lshl_b64 s[38:39], s[64:65], 17
	s_lshl_b64 s[74:75], s[20:21], 10
	v_lshl_add_u64 v[4:5], v[166:167], 0, s[38:39]
	v_lshl_add_u64 v[4:5], v[4:5], 0, s[74:75]
	s_waitcnt vmcnt(10)
	v_add_co_u32_e32 v94, vcc, 0x2000, v4
	s_nop 1
	v_addc_co_u32_e32 v95, vcc, 0, v5, vcc
	global_load_dwordx4 v[126:129], v[4:5], off
	global_load_dwordx4 v[130:133], v[94:95], off
	s_waitcnt vmcnt(7) lgkmcnt(2)
	v_mfma_f32_16x16x32_bf16 v[102:105], v[146:149], v[14:17], v[102:105]
	s_waitcnt vmcnt(5)
	v_mfma_f32_16x16x32_bf16 v[98:101], v[122:125], v[14:17], v[98:101]
	s_waitcnt lgkmcnt(1)
	v_mfma_f32_16x16x32_bf16 v[90:93], v[146:149], v[18:21], v[90:93]
	v_mfma_f32_16x16x32_bf16 v[86:89], v[122:125], v[18:21], v[86:89]
	s_waitcnt lgkmcnt(0)
	v_mfma_f32_16x16x32_bf16 v[74:77], v[146:149], v[26:29], v[74:77]
	v_mfma_f32_16x16x32_bf16 v[70:73], v[122:125], v[26:29], v[70:73]
.LBB0_1432:
	s_waitcnt lgkmcnt(1)
	ds_read_b128 v[18:21], v3 offset:28672
	ds_read_b128 v[14:17], v3 offset:24576
	s_waitcnt lgkmcnt(2)
	ds_read_b128 v[26:29], v3 offset:32768
.LBB0_1434:
	global_load_dwordx4 v[114:117], v[4:5], off offset:1024
	s_waitcnt vmcnt(8) lgkmcnt(1)
	v_mfma_f32_16x16x32_bf16 v[82:85], v[146:149], v[158:161], v[82:85]
	s_waitcnt vmcnt(6)
	v_mfma_f32_16x16x32_bf16 v[78:81], v[122:125], v[158:161], v[78:81]
	v_mfma_f32_16x16x32_bf16 v[66:69], v[146:149], v[154:157], v[66:69]
	v_mfma_f32_16x16x32_bf16 v[62:65], v[122:125], v[154:157], v[62:65]
	s_waitcnt lgkmcnt(0)
	v_mfma_f32_16x16x32_bf16 v[50:53], v[146:149], v[162:165], v[50:53]
	v_mfma_f32_16x16x32_bf16 v[46:49], v[122:125], v[162:165], v[46:49]
.LBB0_1436:
	v_add_u32_e32 v3, v172, v174
	s_waitcnt lgkmcnt(1)
	ds_read_b128 v[158:161], v3
	ds_read_b128 v[154:157], v3 offset:4096
	s_waitcnt lgkmcnt(2)
	ds_read_b128 v[162:165], v3 offset:8192
.LBB0_1438:
	global_load_dwordx4 v[106:109], v[4:5], off offset:2048
	s_waitcnt vmcnt(9) lgkmcnt(1)
	v_mfma_f32_16x16x32_bf16 v[58:61], v[146:149], v[14:17], v[58:61]
	s_waitcnt vmcnt(7)
	v_mfma_f32_16x16x32_bf16 v[54:57], v[122:125], v[14:17], v[54:57]
	v_mfma_f32_16x16x32_bf16 v[42:45], v[146:149], v[18:21], v[42:45]
	v_mfma_f32_16x16x32_bf16 v[38:41], v[122:125], v[18:21], v[38:41]
	s_waitcnt lgkmcnt(0)
	v_mfma_f32_16x16x32_bf16 v[34:37], v[146:149], v[26:29], v[34:37]
	v_mfma_f32_16x16x32_bf16 v[30:33], v[122:125], v[26:29], v[30:33]
.LBB0_1440:
	s_waitcnt lgkmcnt(1)
	ds_read_b128 v[14:17], v3 offset:12288
	ds_read_b128 v[18:21], v3 offset:16384
	s_waitcnt lgkmcnt(2)
	ds_read_b128 v[26:29], v3 offset:20480
.LBB0_1442:
	v_add_co_u32_e32 v94, vcc, 0x2000, v4
	s_nop 1
	v_addc_co_u32_e32 v95, vcc, 0, v5, vcc
	global_load_dwordx4 v[122:125], v[94:95], off offset:1024
	s_waitcnt vmcnt(9) lgkmcnt(1)
	v_mfma_f32_16x16x32_bf16 v[102:105], v[138:141], v[158:161], v[102:105]
	s_waitcnt vmcnt(6)
	v_mfma_f32_16x16x32_bf16 v[98:101], v[150:153], v[158:161], v[98:101]
	v_mfma_f32_16x16x32_bf16 v[90:93], v[138:141], v[154:157], v[90:93]
	v_mfma_f32_16x16x32_bf16 v[86:89], v[150:153], v[154:157], v[86:89]
	s_waitcnt lgkmcnt(0)
	v_mfma_f32_16x16x32_bf16 v[74:77], v[138:141], v[162:165], v[74:77]
	v_mfma_f32_16x16x32_bf16 v[70:73], v[150:153], v[162:165], v[70:73]

.LBB0_1446:
	global_load_dwordx4 v[94:97], v[4:5], off offset:3072
	s_waitcnt vmcnt(10) lgkmcnt(1)
	v_mfma_f32_16x16x32_bf16 v[82:85], v[138:141], v[14:17], v[82:85]
	s_waitcnt vmcnt(7)
	v_mfma_f32_16x16x32_bf16 v[78:81], v[150:153], v[14:17], v[78:81]
	v_mfma_f32_16x16x32_bf16 v[66:69], v[138:141], v[18:21], v[66:69]
	v_mfma_f32_16x16x32_bf16 v[62:65], v[150:153], v[18:21], v[62:65]
	s_waitcnt lgkmcnt(0)
	v_mfma_f32_16x16x32_bf16 v[50:53], v[138:141], v[26:29], v[50:53]
	v_mfma_f32_16x16x32_bf16 v[46:49], v[150:153], v[26:29], v[46:49]
.LBB0_1448:
	v_add_u32_e32 v3, v172, v175
	s_waitcnt lgkmcnt(1)
	ds_read_b128 v[14:17], v3
	ds_read_b128 v[18:21], v3 offset:4096
	s_waitcnt lgkmcnt(2)
	ds_read_b128 v[26:29], v3 offset:8192
.LBB0_1450:
	s_waitcnt vmcnt(14)
	v_add_co_u32_e32 v110, vcc, 0x2000, v4
	s_nop 1
	v_addc_co_u32_e32 v111, vcc, 0, v5, vcc
	global_load_dwordx4 v[118:121], v[110:111], off offset:2048
	s_waitcnt vmcnt(11) lgkmcnt(1)
	v_mfma_f32_16x16x32_bf16 v[58:61], v[138:141], v[158:161], v[58:61]
	s_waitcnt vmcnt(8)
	v_mfma_f32_16x16x32_bf16 v[54:57], v[150:153], v[158:161], v[54:57]
	v_mfma_f32_16x16x32_bf16 v[42:45], v[138:141], v[154:157], v[42:45]
	v_mfma_f32_16x16x32_bf16 v[38:41], v[150:153], v[154:157], v[38:41]
	s_waitcnt lgkmcnt(0)
	v_mfma_f32_16x16x32_bf16 v[34:37], v[138:141], v[162:165], v[34:37]
	v_mfma_f32_16x16x32_bf16 v[30:33], v[150:153], v[162:165], v[30:33]

.LBB0_1454:
	v_add_co_u32_e32 v4, vcc, 0x2000, v4
	s_nop 1
	v_addc_co_u32_e32 v5, vcc, 0, v5, vcc
	global_load_dwordx4 v[110:113], v[4:5], off offset:3072
	s_waitcnt vmcnt(10) lgkmcnt(1)
	v_mfma_f32_16x16x32_bf16 v[102:105], v[134:137], v[14:17], v[102:105]
	s_waitcnt vmcnt(8)
	v_mfma_f32_16x16x32_bf16 v[98:101], v[142:145], v[14:17], v[98:101]
	v_mfma_f32_16x16x32_bf16 v[90:93], v[134:137], v[18:21], v[90:93]
	v_mfma_f32_16x16x32_bf16 v[86:89], v[142:145], v[18:21], v[86:89]
	s_waitcnt lgkmcnt(0)
	v_mfma_f32_16x16x32_bf16 v[74:77], v[134:137], v[26:29], v[74:77]
	v_mfma_f32_16x16x32_bf16 v[70:73], v[142:145], v[26:29], v[70:73]

.LBB0_1458:
	s_waitcnt vmcnt(10) lgkmcnt(1)
	v_mfma_f32_16x16x32_bf16 v[82:85], v[134:137], v[158:161], v[82:85]
	s_waitcnt vmcnt(8)
	v_mfma_f32_16x16x32_bf16 v[78:81], v[142:145], v[158:161], v[78:81]
	v_mfma_f32_16x16x32_bf16 v[66:69], v[134:137], v[154:157], v[66:69]
	v_mfma_f32_16x16x32_bf16 v[62:65], v[142:145], v[154:157], v[62:65]
	s_waitcnt lgkmcnt(0)
	v_mfma_f32_16x16x32_bf16 v[50:53], v[134:137], v[162:165], v[50:53]
	v_mfma_f32_16x16x32_bf16 v[46:49], v[142:145], v[162:165], v[46:49]
.LBB0_1460:
	s_waitcnt vmcnt(10) lgkmcnt(1)
	v_mfma_f32_16x16x32_bf16 v[58:61], v[134:137], v[14:17], v[58:61]
	s_waitcnt vmcnt(8)
	v_mfma_f32_16x16x32_bf16 v[54:57], v[142:145], v[14:17], v[54:57]
	v_mfma_f32_16x16x32_bf16 v[42:45], v[134:137], v[18:21], v[42:45]
	v_mfma_f32_16x16x32_bf16 v[38:41], v[142:145], v[18:21], v[38:41]
	s_waitcnt lgkmcnt(0)
	v_mfma_f32_16x16x32_bf16 v[34:37], v[134:137], v[26:29], v[34:37]
	v_mfma_f32_16x16x32_bf16 v[30:33], v[142:145], v[26:29], v[30:33]
.LBB0_1462:
	v_mov_b32_e32 v3, v168
	v_mov_b32_e32 v4, v169
	s_nop 0
	v_lshlrev_b32_e32 v5, 2, v3
	s_waitcnt vmcnt(10)
	v_add_u32_e32 v134, 0, v5
	v_add_u32_e32 v134, 0x25000, v134
	v_add_u32_e32 v5, s44, v5
	s_waitcnt vmcnt(9)
	ds_read2_b32 v[150:151], v134 offset1:16
	ds_read2_b32 v[148:149], v5 offset0:16 offset1:32
	ds_read2_b32 v[146:147], v134 offset0:32 offset1:48
	s_waitcnt vmcnt(8)
	ds_read2_b32 v[144:145], v5 offset0:48 offset1:64
	ds_read2_b32 v[142:143], v134 offset0:64 offset1:80
	ds_read2_b32 v[140:141], v5 offset0:80 offset1:96
	ds_read2_b32 v[138:139], v134 offset0:96 offset1:112
	ds_read2_b32 v[136:137], v5 offset0:112 offset1:128
	ds_read_b32 v134, v134 offset:512
	v_lshlrev_b32_e32 v4, 3, v4
	v_ashrrev_i32_e32 v5, 31, v4
	s_waitcnt lgkmcnt(8)
	v_cmp_lt_i32_e32 vcc, -1, v150
	s_and_saveexec_b64 s[38:39], vcc
	s_xor_b64 s[38:39], exec, s[38:39]
	s_cbranch_execz .LBB0_1471
	v_lshl_add_u32 v3, v3, 2, 0
	v_add_u32_e32 v3, 0x25280, v3
	ds_read_b32 v152, v3
	s_add_u32 s74, s66, s48
	s_addc_u32 s75, s67, s49
	s_waitcnt lgkmcnt(0)
	v_pk_mul_f32 v[104:105], v[104:105], v[152:153] op_sel_hi:[1,0]
	v_pk_mul_f32 v[102:103], v[102:103], v[152:153] op_sel_hi:[1,0]
	v_pk_mul_f32 v[100:101], v[100:101], v[152:153] op_sel_hi:[1,0]
	v_cvt_pkrtz_f16_f32 v3, v102, v103
	v_cvt_pkrtz_f16_f32 v102, v104, v105
	v_pk_mul_f32 v[98:99], v[98:99], v[152:153] op_sel_hi:[1,0]
	v_add_u32_e32 v3, 0x800080, v3
	v_add_u32_e32 v102, 0x800080, v102
	v_perm_b32 v102, v102, v3, s45
	v_cvt_pkrtz_f16_f32 v3, v98, v99
	v_cvt_pkrtz_f16_f32 v98, v100, v101
	v_add_u32_e32 v3, 0x800080, v3
	v_add_u32_e32 v98, 0x800080, v98
	v_perm_b32 v103, v98, v3, s45
	v_mov_b32_e32 v98, v150
	v_mov_b32_e32 v99, v2
	v_lshlrev_b64 v[98:99], 10, v[98:99]
	v_lshl_add_u64 v[98:99], v[98:99], 0, v[4:5]
	v_lshl_add_u64 v[98:99], s[74:75], 0, v[98:99]
	global_store_dwordx2 v[98:99], v[102:103], off
	s_or_b64 exec, exec, s[38:39]
	v_cmp_lt_i32_e32 vcc, -1, v151
	s_and_saveexec_b64 s[38:39], vcc
	s_cbranch_execnz .LBB0_1472
